# P4 row loads issued before the first wait; P1 int8 row stores write-through (sc1); on top of single-pass P1, P6 router prefetch, P7/P8 epilogue batching
# speedup vs baseline: 1.0139x; 1.0038x over previous
.LBB0_122:
	s_lshr_b32 s3, s33, 10
	s_mul_i32 s8, s3, 0x3000
	s_ashr_i32 s9, s8, 31
	s_lshl_b64 s[8:9], s[8:9], 2
	s_add_u32 s10, s28, s8
	s_addc_u32 s11, s29, s9
	s_lshl_b32 s8, s33, 2
	s_add_u32 s12, s10, 0x2000
	s_addc_u32 s13, s11, 0
	s_or_b32 s24, s8, 1
	s_ashr_i32 s9, s8, 31
	s_ashr_i32 s25, s24, 31
	s_or_b32 s22, s8, 2
	s_or_b32 vcc_lo, s8, 3
	s_lshl_b64 s[14:15], s[8:9], 13
	s_lshl_b64 s[16:17], s[24:25], 13
	s_ashr_i32 s23, s22, 31
	s_ashr_i32 vcc_hi, vcc_lo, 31
	s_waitcnt lgkmcnt(0)
	v_lshlrev_b32_e32 v28, 4, v0
	global_load_dwordx4 v[76:79], v28, s[10:11]
	global_load_dwordx4 v[80:83], v28, s[12:13]
	s_mov_b64 s[44:45], 0x2000
	s_mov_b64 s[16:17], 0x1000
	v_lshl_add_u64 v[2:3], v[30:31], 0, s[14:15]
	v_lshl_add_u64 v[4:5], v[2:3], 0, s[44:45]
	v_lshl_add_u64 v[6:7], v[4:5], 0, s[44:45]
	v_lshl_add_u64 v[8:9], v[6:7], 0, s[44:45]
	v_lshl_add_u64 v[10:11], v[2:3], 0, s[16:17]
	v_lshl_add_u64 v[12:13], v[4:5], 0, s[16:17]
	v_lshl_add_u64 v[14:15], v[6:7], 0, s[16:17]
	v_lshl_add_u64 v[16:17], v[8:9], 0, s[16:17]
	global_load_dwordx4 v[114:117], v[2:3], off
	global_load_dwordx4 v[118:121], v[4:5], off
	global_load_dwordx4 v[122:125], v[6:7], off
	global_load_dwordx4 v[126:129], v[8:9], off
	global_load_dwordx4 v[130:133], v[2:3], off offset:1024
	global_load_dwordx4 v[134:137], v[4:5], off offset:1024
	global_load_dwordx4 v[138:141], v[6:7], off offset:1024
	global_load_dwordx4 v[142:145], v[8:9], off offset:1024
	global_load_dwordx4 v[146:149], v[2:3], off offset:2048
	global_load_dwordx4 v[150:153], v[4:5], off offset:2048
	global_load_dwordx4 v[154:157], v[6:7], off offset:2048
	global_load_dwordx4 v[158:161], v[8:9], off offset:2048
	global_load_dwordx4 v[162:165], v[2:3], off offset:3072
	global_load_dwordx4 v[166:169], v[4:5], off offset:3072
	global_load_dwordx4 v[170:173], v[6:7], off offset:3072
	global_load_dwordx4 v[174:177], v[8:9], off offset:3072
	global_load_dwordx4 v[178:181], v[10:11], off
	global_load_dwordx4 v[182:185], v[12:13], off
	global_load_dwordx4 v[186:189], v[14:15], off
	global_load_dwordx4 v[190:193], v[16:17], off
	global_load_dwordx4 v[194:197], v[10:11], off offset:1024
	global_load_dwordx4 v[198:201], v[12:13], off offset:1024
	global_load_dwordx4 v[202:205], v[14:15], off offset:1024
	global_load_dwordx4 v[206:209], v[16:17], off offset:1024
	global_load_dwordx4 v[210:213], v[10:11], off offset:2048
	global_load_dwordx4 v[216:219], v[12:13], off offset:2048
	global_load_dwordx4 v[220:223], v[14:15], off offset:2048
	global_load_dwordx4 v[224:227], v[16:17], off offset:2048
	global_load_dwordx4 v[228:231], v[10:11], off offset:3072
	global_load_dwordx4 v[232:235], v[12:13], off offset:3072
	global_load_dwordx4 v[236:239], v[14:15], off offset:3072
	global_load_dwordx4 v[240:243], v[16:17], off offset:3072
	v_mov_b32_e32 v71, 0
	v_mov_b32_e32 v72, 0
	v_mov_b32_e32 v73, 0
	v_mov_b32_e32 v74, 0
	v_mov_b32_e32 v39, 0
	v_mov_b32_e32 v40, 0
	v_mov_b32_e32 v41, 0
	v_mov_b32_e32 v42, 0
	v_mov_b32_e32 v43, 0
	v_mov_b32_e32 v44, 0
	v_mov_b32_e32 v45, 0
	v_mov_b32_e32 v46, 0
	v_mov_b32_e32 v47, 0
	v_mov_b32_e32 v48, 0
	v_mov_b32_e32 v49, 0
	v_mov_b32_e32 v50, 0
	v_mov_b32_e32 v51, 0
	v_mov_b32_e32 v52, 0
	v_mov_b32_e32 v53, 0
	v_mov_b32_e32 v54, 0
	v_mov_b32_e32 v55, 0
	v_mov_b32_e32 v56, 0
	v_mov_b32_e32 v57, 0
	v_mov_b32_e32 v58, 0
	v_mov_b32_e32 v59, 0
	v_mov_b32_e32 v60, 0
	v_mov_b32_e32 v61, 0
	v_mov_b32_e32 v62, 0
	v_mov_b32_e32 v63, 0
	v_mov_b32_e32 v64, 0
	v_mov_b32_e32 v65, 0
	v_mov_b32_e32 v66, 0
	v_mov_b32_e32 v67, 0
	v_mov_b32_e32 v68, 0
	v_mov_b32_e32 v69, 0
	v_mov_b32_e32 v70, 0
	v_add_u32_e32 v75, 0x10000, v1
	v_add_u32_e32 v28, 0x10000, v28
	s_waitcnt vmcnt(32)
	v_add_f32_e32 v80, 1.0, v80
	v_add_f32_e32 v81, 1.0, v81
	v_add_f32_e32 v82, 1.0, v82
	v_add_f32_e32 v83, 1.0, v83
	s_barrier
	ds_write_b128 v28, v[76:79]
	ds_write_b128 v28, v[80:83] offset:8192
	s_waitcnt lgkmcnt(0)
	s_barrier
	ds_read_b128 v[76:79], v75 offset:0
	ds_read_b128 v[80:83], v75 offset:8192
	ds_read_b128 v[84:87], v1 offset:0
	s_waitcnt vmcnt(28) lgkmcnt(1)
	v_fma_f32 v114, v114, v80, v76
	v_fma_f32 v115, v115, v81, v77
	v_fma_f32 v116, v116, v82, v78
	v_fma_f32 v117, v117, v83, v79
	v_max3_f32 v71, v71, |v114|, |v115|
	v_max3_f32 v71, v71, |v116|, |v117|
	v_fma_f32 v118, v118, v80, v76
	v_fma_f32 v119, v119, v81, v77
	v_fma_f32 v120, v120, v82, v78
	v_fma_f32 v121, v121, v83, v79
	v_max3_f32 v72, v72, |v118|, |v119|
	v_max3_f32 v72, v72, |v120|, |v121|
	v_fma_f32 v122, v122, v80, v76
	v_fma_f32 v123, v123, v81, v77
	v_fma_f32 v124, v124, v82, v78
	v_fma_f32 v125, v125, v83, v79
	v_max3_f32 v73, v73, |v122|, |v123|
	v_max3_f32 v73, v73, |v124|, |v125|
	v_fma_f32 v126, v126, v80, v76
	v_fma_f32 v127, v127, v81, v77
	v_fma_f32 v128, v128, v82, v78
	v_fma_f32 v129, v129, v83, v79
	v_max3_f32 v74, v74, |v126|, |v127|
	v_max3_f32 v74, v74, |v128|, |v129|
	ds_read_b128 v[88:91], v1 offset:8192
	s_waitcnt lgkmcnt(1)
	v_fmac_f32_e32 v39, v114, v84
	v_fmac_f32_e32 v47, v118, v84
	v_fmac_f32_e32 v55, v122, v84
	v_fmac_f32_e32 v63, v126, v84
	v_fmac_f32_e32 v39, v115, v85
	v_fmac_f32_e32 v47, v119, v85
	v_fmac_f32_e32 v55, v123, v85
	v_fmac_f32_e32 v63, v127, v85
	v_fmac_f32_e32 v39, v116, v86
	v_fmac_f32_e32 v47, v120, v86
	v_fmac_f32_e32 v55, v124, v86
	v_fmac_f32_e32 v63, v128, v86
	v_fmac_f32_e32 v39, v117, v87
	v_fmac_f32_e32 v47, v121, v87
	v_fmac_f32_e32 v55, v125, v87
	v_fmac_f32_e32 v63, v129, v87
	ds_read_b128 v[84:87], v1 offset:16384
	s_waitcnt lgkmcnt(1)
	v_fmac_f32_e32 v40, v114, v88
	v_fmac_f32_e32 v48, v118, v88
	v_fmac_f32_e32 v56, v122, v88
	v_fmac_f32_e32 v64, v126, v88
	v_fmac_f32_e32 v40, v115, v89
	v_fmac_f32_e32 v48, v119, v89
	v_fmac_f32_e32 v56, v123, v89
	v_fmac_f32_e32 v64, v127, v89
	v_fmac_f32_e32 v40, v116, v90
	v_fmac_f32_e32 v48, v120, v90
	v_fmac_f32_e32 v56, v124, v90
	v_fmac_f32_e32 v64, v128, v90
	v_fmac_f32_e32 v40, v117, v91
	v_fmac_f32_e32 v48, v121, v91
	v_fmac_f32_e32 v56, v125, v91
	v_fmac_f32_e32 v64, v129, v91
	ds_read_b128 v[88:91], v1 offset:24576
	s_waitcnt lgkmcnt(1)
	v_fmac_f32_e32 v41, v114, v84
	v_fmac_f32_e32 v49, v118, v84
	v_fmac_f32_e32 v57, v122, v84
	v_fmac_f32_e32 v65, v126, v84
	v_fmac_f32_e32 v41, v115, v85
	v_fmac_f32_e32 v49, v119, v85
	v_fmac_f32_e32 v57, v123, v85
	v_fmac_f32_e32 v65, v127, v85
	v_fmac_f32_e32 v41, v116, v86
	v_fmac_f32_e32 v49, v120, v86
	v_fmac_f32_e32 v57, v124, v86
	v_fmac_f32_e32 v65, v128, v86
	v_fmac_f32_e32 v41, v117, v87
	v_fmac_f32_e32 v49, v121, v87
	v_fmac_f32_e32 v57, v125, v87
	v_fmac_f32_e32 v65, v129, v87
	ds_read_b128 v[84:87], v1 offset:32768
	s_waitcnt lgkmcnt(1)
	v_fmac_f32_e32 v42, v114, v88
	v_fmac_f32_e32 v50, v118, v88
	v_fmac_f32_e32 v58, v122, v88
	v_fmac_f32_e32 v66, v126, v88
	v_fmac_f32_e32 v42, v115, v89
	v_fmac_f32_e32 v50, v119, v89
	v_fmac_f32_e32 v58, v123, v89
	v_fmac_f32_e32 v66, v127, v89
	v_fmac_f32_e32 v42, v116, v90
	v_fmac_f32_e32 v50, v120, v90
	v_fmac_f32_e32 v58, v124, v90
	v_fmac_f32_e32 v66, v128, v90
	v_fmac_f32_e32 v42, v117, v91
	v_fmac_f32_e32 v50, v121, v91
	v_fmac_f32_e32 v58, v125, v91
	v_fmac_f32_e32 v66, v129, v91
	ds_read_b128 v[88:91], v1 offset:40960
	s_waitcnt lgkmcnt(1)
	v_fmac_f32_e32 v43, v114, v84
	v_fmac_f32_e32 v51, v118, v84
	v_fmac_f32_e32 v59, v122, v84
	v_fmac_f32_e32 v67, v126, v84
	v_fmac_f32_e32 v43, v115, v85
	v_fmac_f32_e32 v51, v119, v85
	v_fmac_f32_e32 v59, v123, v85
	v_fmac_f32_e32 v67, v127, v85
	v_fmac_f32_e32 v43, v116, v86
	v_fmac_f32_e32 v51, v120, v86
	v_fmac_f32_e32 v59, v124, v86
	v_fmac_f32_e32 v67, v128, v86
	v_fmac_f32_e32 v43, v117, v87
	v_fmac_f32_e32 v51, v121, v87
	v_fmac_f32_e32 v59, v125, v87
	v_fmac_f32_e32 v67, v129, v87
	ds_read_b128 v[84:87], v1 offset:49152
	s_waitcnt lgkmcnt(1)
	v_fmac_f32_e32 v44, v114, v88
	v_fmac_f32_e32 v52, v118, v88
	v_fmac_f32_e32 v60, v122, v88
	v_fmac_f32_e32 v68, v126, v88
	v_fmac_f32_e32 v44, v115, v89
	v_fmac_f32_e32 v52, v119, v89
	v_fmac_f32_e32 v60, v123, v89
	v_fmac_f32_e32 v68, v127, v89
	v_fmac_f32_e32 v44, v116, v90
	v_fmac_f32_e32 v52, v120, v90
	v_fmac_f32_e32 v60, v124, v90
	v_fmac_f32_e32 v68, v128, v90
	v_fmac_f32_e32 v44, v117, v91
	v_fmac_f32_e32 v52, v121, v91
	v_fmac_f32_e32 v60, v125, v91
	v_fmac_f32_e32 v68, v129, v91
	ds_read_b128 v[88:91], v1 offset:57344
	s_waitcnt lgkmcnt(1)
	v_fmac_f32_e32 v45, v114, v84
	v_fmac_f32_e32 v53, v118, v84
	v_fmac_f32_e32 v61, v122, v84
	v_fmac_f32_e32 v69, v126, v84
	v_fmac_f32_e32 v45, v115, v85
	v_fmac_f32_e32 v53, v119, v85
	v_fmac_f32_e32 v61, v123, v85
	v_fmac_f32_e32 v69, v127, v85
	v_fmac_f32_e32 v45, v116, v86
	v_fmac_f32_e32 v53, v120, v86
	v_fmac_f32_e32 v61, v124, v86
	v_fmac_f32_e32 v69, v128, v86
	v_fmac_f32_e32 v45, v117, v87
	v_fmac_f32_e32 v53, v121, v87
	v_fmac_f32_e32 v61, v125, v87
	v_fmac_f32_e32 v69, v129, v87
	s_waitcnt lgkmcnt(0)
	v_fmac_f32_e32 v46, v114, v88
	v_fmac_f32_e32 v54, v118, v88
	v_fmac_f32_e32 v62, v122, v88
	v_fmac_f32_e32 v70, v126, v88
	v_fmac_f32_e32 v46, v115, v89
	v_fmac_f32_e32 v54, v119, v89
	v_fmac_f32_e32 v62, v123, v89
	v_fmac_f32_e32 v70, v127, v89
	v_fmac_f32_e32 v46, v116, v90
	v_fmac_f32_e32 v54, v120, v90
	v_fmac_f32_e32 v62, v124, v90
	v_fmac_f32_e32 v70, v128, v90
	v_fmac_f32_e32 v46, v117, v91
	v_fmac_f32_e32 v54, v121, v91
	v_fmac_f32_e32 v62, v125, v91
	v_fmac_f32_e32 v70, v129, v91
	ds_read_b128 v[76:79], v75 offset:1024
	ds_read_b128 v[80:83], v75 offset:9216
	ds_read_b128 v[84:87], v1 offset:1024
	s_waitcnt vmcnt(24) lgkmcnt(1)
	v_fma_f32 v130, v130, v80, v76
	v_fma_f32 v131, v131, v81, v77
	v_fma_f32 v132, v132, v82, v78
	v_fma_f32 v133, v133, v83, v79
	v_max3_f32 v71, v71, |v130|, |v131|
	v_max3_f32 v71, v71, |v132|, |v133|
	v_fma_f32 v134, v134, v80, v76
	v_fma_f32 v135, v135, v81, v77
	v_fma_f32 v136, v136, v82, v78
	v_fma_f32 v137, v137, v83, v79
	v_max3_f32 v72, v72, |v134|, |v135|
	v_max3_f32 v72, v72, |v136|, |v137|
	v_fma_f32 v138, v138, v80, v76
	v_fma_f32 v139, v139, v81, v77
	v_fma_f32 v140, v140, v82, v78
	v_fma_f32 v141, v141, v83, v79
	v_max3_f32 v73, v73, |v138|, |v139|
	v_max3_f32 v73, v73, |v140|, |v141|
	v_fma_f32 v142, v142, v80, v76
	v_fma_f32 v143, v143, v81, v77
	v_fma_f32 v144, v144, v82, v78
	v_fma_f32 v145, v145, v83, v79
	v_max3_f32 v74, v74, |v142|, |v143|
	v_max3_f32 v74, v74, |v144|, |v145|
	ds_read_b128 v[88:91], v1 offset:9216
	s_waitcnt lgkmcnt(1)
	v_fmac_f32_e32 v39, v130, v84
	v_fmac_f32_e32 v47, v134, v84
	v_fmac_f32_e32 v55, v138, v84
	v_fmac_f32_e32 v63, v142, v84
	v_fmac_f32_e32 v39, v131, v85
	v_fmac_f32_e32 v47, v135, v85
	v_fmac_f32_e32 v55, v139, v85
	v_fmac_f32_e32 v63, v143, v85
	v_fmac_f32_e32 v39, v132, v86
	v_fmac_f32_e32 v47, v136, v86
	v_fmac_f32_e32 v55, v140, v86
	v_fmac_f32_e32 v63, v144, v86
	v_fmac_f32_e32 v39, v133, v87
	v_fmac_f32_e32 v47, v137, v87
	v_fmac_f32_e32 v55, v141, v87
	v_fmac_f32_e32 v63, v145, v87
	ds_read_b128 v[84:87], v1 offset:17408
	s_waitcnt lgkmcnt(1)
	v_fmac_f32_e32 v40, v130, v88
	v_fmac_f32_e32 v48, v134, v88
	v_fmac_f32_e32 v56, v138, v88
	v_fmac_f32_e32 v64, v142, v88
	v_fmac_f32_e32 v40, v131, v89
	v_fmac_f32_e32 v48, v135, v89
	v_fmac_f32_e32 v56, v139, v89
	v_fmac_f32_e32 v64, v143, v89
	v_fmac_f32_e32 v40, v132, v90
	v_fmac_f32_e32 v48, v136, v90
	v_fmac_f32_e32 v56, v140, v90
	v_fmac_f32_e32 v64, v144, v90
	v_fmac_f32_e32 v40, v133, v91
	v_fmac_f32_e32 v48, v137, v91
	v_fmac_f32_e32 v56, v141, v91
	v_fmac_f32_e32 v64, v145, v91
	ds_read_b128 v[88:91], v1 offset:25600
	s_waitcnt lgkmcnt(1)
	v_fmac_f32_e32 v41, v130, v84
	v_fmac_f32_e32 v49, v134, v84
	v_fmac_f32_e32 v57, v138, v84
	v_fmac_f32_e32 v65, v142, v84
	v_fmac_f32_e32 v41, v131, v85
	v_fmac_f32_e32 v49, v135, v85
	v_fmac_f32_e32 v57, v139, v85
	v_fmac_f32_e32 v65, v143, v85
	v_fmac_f32_e32 v41, v132, v86
	v_fmac_f32_e32 v49, v136, v86
	v_fmac_f32_e32 v57, v140, v86
	v_fmac_f32_e32 v65, v144, v86
	v_fmac_f32_e32 v41, v133, v87
	v_fmac_f32_e32 v49, v137, v87
	v_fmac_f32_e32 v57, v141, v87
	v_fmac_f32_e32 v65, v145, v87
	ds_read_b128 v[84:87], v1 offset:33792
	s_waitcnt lgkmcnt(1)
	v_fmac_f32_e32 v42, v130, v88
	v_fmac_f32_e32 v50, v134, v88
	v_fmac_f32_e32 v58, v138, v88
	v_fmac_f32_e32 v66, v142, v88
	v_fmac_f32_e32 v42, v131, v89
	v_fmac_f32_e32 v50, v135, v89
	v_fmac_f32_e32 v58, v139, v89
	v_fmac_f32_e32 v66, v143, v89
	v_fmac_f32_e32 v42, v132, v90
	v_fmac_f32_e32 v50, v136, v90
	v_fmac_f32_e32 v58, v140, v90
	v_fmac_f32_e32 v66, v144, v90
	v_fmac_f32_e32 v42, v133, v91
	v_fmac_f32_e32 v50, v137, v91
	v_fmac_f32_e32 v58, v141, v91
	v_fmac_f32_e32 v66, v145, v91
	ds_read_b128 v[88:91], v1 offset:41984
	s_waitcnt lgkmcnt(1)
	v_fmac_f32_e32 v43, v130, v84
	v_fmac_f32_e32 v51, v134, v84
	v_fmac_f32_e32 v59, v138, v84
	v_fmac_f32_e32 v67, v142, v84
	v_fmac_f32_e32 v43, v131, v85
	v_fmac_f32_e32 v51, v135, v85
	v_fmac_f32_e32 v59, v139, v85
	v_fmac_f32_e32 v67, v143, v85
	v_fmac_f32_e32 v43, v132, v86
	v_fmac_f32_e32 v51, v136, v86
	v_fmac_f32_e32 v59, v140, v86
	v_fmac_f32_e32 v67, v144, v86
	v_fmac_f32_e32 v43, v133, v87
	v_fmac_f32_e32 v51, v137, v87
	v_fmac_f32_e32 v59, v141, v87
	v_fmac_f32_e32 v67, v145, v87
	ds_read_b128 v[84:87], v1 offset:50176
	s_waitcnt lgkmcnt(1)
	v_fmac_f32_e32 v44, v130, v88
	v_fmac_f32_e32 v52, v134, v88
	v_fmac_f32_e32 v60, v138, v88
	v_fmac_f32_e32 v68, v142, v88
	v_fmac_f32_e32 v44, v131, v89
	v_fmac_f32_e32 v52, v135, v89
	v_fmac_f32_e32 v60, v139, v89
	v_fmac_f32_e32 v68, v143, v89
	v_fmac_f32_e32 v44, v132, v90
	v_fmac_f32_e32 v52, v136, v90
	v_fmac_f32_e32 v60, v140, v90
	v_fmac_f32_e32 v68, v144, v90
	v_fmac_f32_e32 v44, v133, v91
	v_fmac_f32_e32 v52, v137, v91
	v_fmac_f32_e32 v60, v141, v91
	v_fmac_f32_e32 v68, v145, v91
	ds_read_b128 v[88:91], v1 offset:58368
	s_waitcnt lgkmcnt(1)
	v_fmac_f32_e32 v45, v130, v84
	v_fmac_f32_e32 v53, v134, v84
	v_fmac_f32_e32 v61, v138, v84
	v_fmac_f32_e32 v69, v142, v84
	v_fmac_f32_e32 v45, v131, v85
	v_fmac_f32_e32 v53, v135, v85
	v_fmac_f32_e32 v61, v139, v85
	v_fmac_f32_e32 v69, v143, v85
	v_fmac_f32_e32 v45, v132, v86
	v_fmac_f32_e32 v53, v136, v86
	v_fmac_f32_e32 v61, v140, v86
	v_fmac_f32_e32 v69, v144, v86
	v_fmac_f32_e32 v45, v133, v87
	v_fmac_f32_e32 v53, v137, v87
	v_fmac_f32_e32 v61, v141, v87
	v_fmac_f32_e32 v69, v145, v87
	s_waitcnt lgkmcnt(0)
	v_fmac_f32_e32 v46, v130, v88
	v_fmac_f32_e32 v54, v134, v88
	v_fmac_f32_e32 v62, v138, v88
	v_fmac_f32_e32 v70, v142, v88
	v_fmac_f32_e32 v46, v131, v89
	v_fmac_f32_e32 v54, v135, v89
	v_fmac_f32_e32 v62, v139, v89
	v_fmac_f32_e32 v70, v143, v89
	v_fmac_f32_e32 v46, v132, v90
	v_fmac_f32_e32 v54, v136, v90
	v_fmac_f32_e32 v62, v140, v90
	v_fmac_f32_e32 v70, v144, v90
	v_fmac_f32_e32 v46, v133, v91
	v_fmac_f32_e32 v54, v137, v91
	v_fmac_f32_e32 v62, v141, v91
	v_fmac_f32_e32 v70, v145, v91
	ds_read_b128 v[76:79], v75 offset:2048
	ds_read_b128 v[80:83], v75 offset:10240
	ds_read_b128 v[84:87], v1 offset:2048
	s_waitcnt vmcnt(20) lgkmcnt(1)
	v_fma_f32 v146, v146, v80, v76
	v_fma_f32 v147, v147, v81, v77
	v_fma_f32 v148, v148, v82, v78
	v_fma_f32 v149, v149, v83, v79
	v_max3_f32 v71, v71, |v146|, |v147|
	v_max3_f32 v71, v71, |v148|, |v149|
	v_fma_f32 v150, v150, v80, v76
	v_fma_f32 v151, v151, v81, v77
	v_fma_f32 v152, v152, v82, v78
	v_fma_f32 v153, v153, v83, v79
	v_max3_f32 v72, v72, |v150|, |v151|
	v_max3_f32 v72, v72, |v152|, |v153|
	v_fma_f32 v154, v154, v80, v76
	v_fma_f32 v155, v155, v81, v77
	v_fma_f32 v156, v156, v82, v78
	v_fma_f32 v157, v157, v83, v79
	v_max3_f32 v73, v73, |v154|, |v155|
	v_max3_f32 v73, v73, |v156|, |v157|
	v_fma_f32 v158, v158, v80, v76
	v_fma_f32 v159, v159, v81, v77
	v_fma_f32 v160, v160, v82, v78
	v_fma_f32 v161, v161, v83, v79
	v_max3_f32 v74, v74, |v158|, |v159|
	v_max3_f32 v74, v74, |v160|, |v161|
	ds_read_b128 v[88:91], v1 offset:10240
	s_waitcnt lgkmcnt(1)
	v_fmac_f32_e32 v39, v146, v84
	v_fmac_f32_e32 v47, v150, v84
	v_fmac_f32_e32 v55, v154, v84
	v_fmac_f32_e32 v63, v158, v84
	v_fmac_f32_e32 v39, v147, v85
	v_fmac_f32_e32 v47, v151, v85
	v_fmac_f32_e32 v55, v155, v85
	v_fmac_f32_e32 v63, v159, v85
	v_fmac_f32_e32 v39, v148, v86
	v_fmac_f32_e32 v47, v152, v86
	v_fmac_f32_e32 v55, v156, v86
	v_fmac_f32_e32 v63, v160, v86
	v_fmac_f32_e32 v39, v149, v87
	v_fmac_f32_e32 v47, v153, v87
	v_fmac_f32_e32 v55, v157, v87
	v_fmac_f32_e32 v63, v161, v87
	ds_read_b128 v[84:87], v1 offset:18432
	s_waitcnt lgkmcnt(1)
	v_fmac_f32_e32 v40, v146, v88
	v_fmac_f32_e32 v48, v150, v88
	v_fmac_f32_e32 v56, v154, v88
	v_fmac_f32_e32 v64, v158, v88
	v_fmac_f32_e32 v40, v147, v89
	v_fmac_f32_e32 v48, v151, v89
	v_fmac_f32_e32 v56, v155, v89
	v_fmac_f32_e32 v64, v159, v89
	v_fmac_f32_e32 v40, v148, v90
	v_fmac_f32_e32 v48, v152, v90
	v_fmac_f32_e32 v56, v156, v90
	v_fmac_f32_e32 v64, v160, v90
	v_fmac_f32_e32 v40, v149, v91
	v_fmac_f32_e32 v48, v153, v91
	v_fmac_f32_e32 v56, v157, v91
	v_fmac_f32_e32 v64, v161, v91
	ds_read_b128 v[88:91], v1 offset:26624
	s_waitcnt lgkmcnt(1)
	v_fmac_f32_e32 v41, v146, v84
	v_fmac_f32_e32 v49, v150, v84
	v_fmac_f32_e32 v57, v154, v84
	v_fmac_f32_e32 v65, v158, v84
	v_fmac_f32_e32 v41, v147, v85
	v_fmac_f32_e32 v49, v151, v85
	v_fmac_f32_e32 v57, v155, v85
	v_fmac_f32_e32 v65, v159, v85
	v_fmac_f32_e32 v41, v148, v86
	v_fmac_f32_e32 v49, v152, v86
	v_fmac_f32_e32 v57, v156, v86
	v_fmac_f32_e32 v65, v160, v86
	v_fmac_f32_e32 v41, v149, v87
	v_fmac_f32_e32 v49, v153, v87
	v_fmac_f32_e32 v57, v157, v87
	v_fmac_f32_e32 v65, v161, v87
	ds_read_b128 v[84:87], v1 offset:34816
	s_waitcnt lgkmcnt(1)
	v_fmac_f32_e32 v42, v146, v88
	v_fmac_f32_e32 v50, v150, v88
	v_fmac_f32_e32 v58, v154, v88
	v_fmac_f32_e32 v66, v158, v88
	v_fmac_f32_e32 v42, v147, v89
	v_fmac_f32_e32 v50, v151, v89
	v_fmac_f32_e32 v58, v155, v89
	v_fmac_f32_e32 v66, v159, v89
	v_fmac_f32_e32 v42, v148, v90
	v_fmac_f32_e32 v50, v152, v90
	v_fmac_f32_e32 v58, v156, v90
	v_fmac_f32_e32 v66, v160, v90
	v_fmac_f32_e32 v42, v149, v91
	v_fmac_f32_e32 v50, v153, v91
	v_fmac_f32_e32 v58, v157, v91
	v_fmac_f32_e32 v66, v161, v91
	ds_read_b128 v[88:91], v1 offset:43008
	s_waitcnt lgkmcnt(1)
	v_fmac_f32_e32 v43, v146, v84
	v_fmac_f32_e32 v51, v150, v84
	v_fmac_f32_e32 v59, v154, v84
	v_fmac_f32_e32 v67, v158, v84
	v_fmac_f32_e32 v43, v147, v85
	v_fmac_f32_e32 v51, v151, v85
	v_fmac_f32_e32 v59, v155, v85
	v_fmac_f32_e32 v67, v159, v85
	v_fmac_f32_e32 v43, v148, v86
	v_fmac_f32_e32 v51, v152, v86
	v_fmac_f32_e32 v59, v156, v86
	v_fmac_f32_e32 v67, v160, v86
	v_fmac_f32_e32 v43, v149, v87
	v_fmac_f32_e32 v51, v153, v87
	v_fmac_f32_e32 v59, v157, v87
	v_fmac_f32_e32 v67, v161, v87
	ds_read_b128 v[84:87], v1 offset:51200
	s_waitcnt lgkmcnt(1)
	v_fmac_f32_e32 v44, v146, v88
	v_fmac_f32_e32 v52, v150, v88
	v_fmac_f32_e32 v60, v154, v88
	v_fmac_f32_e32 v68, v158, v88
	v_fmac_f32_e32 v44, v147, v89
	v_fmac_f32_e32 v52, v151, v89
	v_fmac_f32_e32 v60, v155, v89
	v_fmac_f32_e32 v68, v159, v89
	v_fmac_f32_e32 v44, v148, v90
	v_fmac_f32_e32 v52, v152, v90
	v_fmac_f32_e32 v60, v156, v90
	v_fmac_f32_e32 v68, v160, v90
	v_fmac_f32_e32 v44, v149, v91
	v_fmac_f32_e32 v52, v153, v91
	v_fmac_f32_e32 v60, v157, v91
	v_fmac_f32_e32 v68, v161, v91
	ds_read_b128 v[88:91], v1 offset:59392
	s_waitcnt lgkmcnt(1)
	v_fmac_f32_e32 v45, v146, v84
	v_fmac_f32_e32 v53, v150, v84
	v_fmac_f32_e32 v61, v154, v84
	v_fmac_f32_e32 v69, v158, v84
	v_fmac_f32_e32 v45, v147, v85
	v_fmac_f32_e32 v53, v151, v85
	v_fmac_f32_e32 v61, v155, v85
	v_fmac_f32_e32 v69, v159, v85
	v_fmac_f32_e32 v45, v148, v86
	v_fmac_f32_e32 v53, v152, v86
	v_fmac_f32_e32 v61, v156, v86
	v_fmac_f32_e32 v69, v160, v86
	v_fmac_f32_e32 v45, v149, v87
	v_fmac_f32_e32 v53, v153, v87
	v_fmac_f32_e32 v61, v157, v87
	v_fmac_f32_e32 v69, v161, v87
	s_waitcnt lgkmcnt(0)
	v_fmac_f32_e32 v46, v146, v88
	v_fmac_f32_e32 v54, v150, v88
	v_fmac_f32_e32 v62, v154, v88
	v_fmac_f32_e32 v70, v158, v88
	v_fmac_f32_e32 v46, v147, v89
	v_fmac_f32_e32 v54, v151, v89
	v_fmac_f32_e32 v62, v155, v89
	v_fmac_f32_e32 v70, v159, v89
	v_fmac_f32_e32 v46, v148, v90
	v_fmac_f32_e32 v54, v152, v90
	v_fmac_f32_e32 v62, v156, v90
	v_fmac_f32_e32 v70, v160, v90
	v_fmac_f32_e32 v46, v149, v91
	v_fmac_f32_e32 v54, v153, v91
	v_fmac_f32_e32 v62, v157, v91
	v_fmac_f32_e32 v70, v161, v91
	ds_read_b128 v[76:79], v75 offset:3072
	ds_read_b128 v[80:83], v75 offset:11264
	ds_read_b128 v[84:87], v1 offset:3072
	s_waitcnt vmcnt(16) lgkmcnt(1)
	v_fma_f32 v162, v162, v80, v76
	v_fma_f32 v163, v163, v81, v77
	v_fma_f32 v164, v164, v82, v78
	v_fma_f32 v165, v165, v83, v79
	v_max3_f32 v71, v71, |v162|, |v163|
	v_max3_f32 v71, v71, |v164|, |v165|
	v_fma_f32 v166, v166, v80, v76
	v_fma_f32 v167, v167, v81, v77
	v_fma_f32 v168, v168, v82, v78
	v_fma_f32 v169, v169, v83, v79
	v_max3_f32 v72, v72, |v166|, |v167|
	v_max3_f32 v72, v72, |v168|, |v169|
	v_fma_f32 v170, v170, v80, v76
	v_fma_f32 v171, v171, v81, v77
	v_fma_f32 v172, v172, v82, v78
	v_fma_f32 v173, v173, v83, v79
	v_max3_f32 v73, v73, |v170|, |v171|
	v_max3_f32 v73, v73, |v172|, |v173|
	v_fma_f32 v174, v174, v80, v76
	v_fma_f32 v175, v175, v81, v77
	v_fma_f32 v176, v176, v82, v78
	v_fma_f32 v177, v177, v83, v79
	v_max3_f32 v74, v74, |v174|, |v175|
	v_max3_f32 v74, v74, |v176|, |v177|
	ds_read_b128 v[88:91], v1 offset:11264
	s_waitcnt lgkmcnt(1)
	v_fmac_f32_e32 v39, v162, v84
	v_fmac_f32_e32 v47, v166, v84
	v_fmac_f32_e32 v55, v170, v84
	v_fmac_f32_e32 v63, v174, v84
	v_fmac_f32_e32 v39, v163, v85
	v_fmac_f32_e32 v47, v167, v85
	v_fmac_f32_e32 v55, v171, v85
	v_fmac_f32_e32 v63, v175, v85
	v_fmac_f32_e32 v39, v164, v86
	v_fmac_f32_e32 v47, v168, v86
	v_fmac_f32_e32 v55, v172, v86
	v_fmac_f32_e32 v63, v176, v86
	v_fmac_f32_e32 v39, v165, v87
	v_fmac_f32_e32 v47, v169, v87
	v_fmac_f32_e32 v55, v173, v87
	v_fmac_f32_e32 v63, v177, v87
	ds_read_b128 v[84:87], v1 offset:19456
	s_waitcnt lgkmcnt(1)
	v_fmac_f32_e32 v40, v162, v88
	v_fmac_f32_e32 v48, v166, v88
	v_fmac_f32_e32 v56, v170, v88
	v_fmac_f32_e32 v64, v174, v88
	v_fmac_f32_e32 v40, v163, v89
	v_fmac_f32_e32 v48, v167, v89
	v_fmac_f32_e32 v56, v171, v89
	v_fmac_f32_e32 v64, v175, v89
	v_fmac_f32_e32 v40, v164, v90
	v_fmac_f32_e32 v48, v168, v90
	v_fmac_f32_e32 v56, v172, v90
	v_fmac_f32_e32 v64, v176, v90
	v_fmac_f32_e32 v40, v165, v91
	v_fmac_f32_e32 v48, v169, v91
	v_fmac_f32_e32 v56, v173, v91
	v_fmac_f32_e32 v64, v177, v91
	ds_read_b128 v[88:91], v1 offset:27648
	s_waitcnt lgkmcnt(1)
	v_fmac_f32_e32 v41, v162, v84
	v_fmac_f32_e32 v49, v166, v84
	v_fmac_f32_e32 v57, v170, v84
	v_fmac_f32_e32 v65, v174, v84
	v_fmac_f32_e32 v41, v163, v85
	v_fmac_f32_e32 v49, v167, v85
	v_fmac_f32_e32 v57, v171, v85
	v_fmac_f32_e32 v65, v175, v85
	v_fmac_f32_e32 v41, v164, v86
	v_fmac_f32_e32 v49, v168, v86
	v_fmac_f32_e32 v57, v172, v86
	v_fmac_f32_e32 v65, v176, v86
	v_fmac_f32_e32 v41, v165, v87
	v_fmac_f32_e32 v49, v169, v87
	v_fmac_f32_e32 v57, v173, v87
	v_fmac_f32_e32 v65, v177, v87
	ds_read_b128 v[84:87], v1 offset:35840
	s_waitcnt lgkmcnt(1)
	v_fmac_f32_e32 v42, v162, v88
	v_fmac_f32_e32 v50, v166, v88
	v_fmac_f32_e32 v58, v170, v88
	v_fmac_f32_e32 v66, v174, v88
	v_fmac_f32_e32 v42, v163, v89
	v_fmac_f32_e32 v50, v167, v89
	v_fmac_f32_e32 v58, v171, v89
	v_fmac_f32_e32 v66, v175, v89
	v_fmac_f32_e32 v42, v164, v90
	v_fmac_f32_e32 v50, v168, v90
	v_fmac_f32_e32 v58, v172, v90
	v_fmac_f32_e32 v66, v176, v90
	v_fmac_f32_e32 v42, v165, v91
	v_fmac_f32_e32 v50, v169, v91
	v_fmac_f32_e32 v58, v173, v91
	v_fmac_f32_e32 v66, v177, v91
	ds_read_b128 v[88:91], v1 offset:44032
	s_waitcnt lgkmcnt(1)
	v_fmac_f32_e32 v43, v162, v84
	v_fmac_f32_e32 v51, v166, v84
	v_fmac_f32_e32 v59, v170, v84
	v_fmac_f32_e32 v67, v174, v84
	v_fmac_f32_e32 v43, v163, v85
	v_fmac_f32_e32 v51, v167, v85
	v_fmac_f32_e32 v59, v171, v85
	v_fmac_f32_e32 v67, v175, v85
	v_fmac_f32_e32 v43, v164, v86
	v_fmac_f32_e32 v51, v168, v86
	v_fmac_f32_e32 v59, v172, v86
	v_fmac_f32_e32 v67, v176, v86
	v_fmac_f32_e32 v43, v165, v87
	v_fmac_f32_e32 v51, v169, v87
	v_fmac_f32_e32 v59, v173, v87
	v_fmac_f32_e32 v67, v177, v87
	ds_read_b128 v[84:87], v1 offset:52224
	s_waitcnt lgkmcnt(1)
	v_fmac_f32_e32 v44, v162, v88
	v_fmac_f32_e32 v52, v166, v88
	v_fmac_f32_e32 v60, v170, v88
	v_fmac_f32_e32 v68, v174, v88
	v_fmac_f32_e32 v44, v163, v89
	v_fmac_f32_e32 v52, v167, v89
	v_fmac_f32_e32 v60, v171, v89
	v_fmac_f32_e32 v68, v175, v89
	v_fmac_f32_e32 v44, v164, v90
	v_fmac_f32_e32 v52, v168, v90
	v_fmac_f32_e32 v60, v172, v90
	v_fmac_f32_e32 v68, v176, v90
	v_fmac_f32_e32 v44, v165, v91
	v_fmac_f32_e32 v52, v169, v91
	v_fmac_f32_e32 v60, v173, v91
	v_fmac_f32_e32 v68, v177, v91
	ds_read_b128 v[88:91], v1 offset:60416
	s_waitcnt lgkmcnt(1)
	v_fmac_f32_e32 v45, v162, v84
	v_fmac_f32_e32 v53, v166, v84
	v_fmac_f32_e32 v61, v170, v84
	v_fmac_f32_e32 v69, v174, v84
	v_fmac_f32_e32 v45, v163, v85
	v_fmac_f32_e32 v53, v167, v85
	v_fmac_f32_e32 v61, v171, v85
	v_fmac_f32_e32 v69, v175, v85
	v_fmac_f32_e32 v45, v164, v86
	v_fmac_f32_e32 v53, v168, v86
	v_fmac_f32_e32 v61, v172, v86
	v_fmac_f32_e32 v69, v176, v86
	v_fmac_f32_e32 v45, v165, v87
	v_fmac_f32_e32 v53, v169, v87
	v_fmac_f32_e32 v61, v173, v87
	v_fmac_f32_e32 v69, v177, v87
	s_waitcnt lgkmcnt(0)
	v_fmac_f32_e32 v46, v162, v88
	v_fmac_f32_e32 v54, v166, v88
	v_fmac_f32_e32 v62, v170, v88
	v_fmac_f32_e32 v70, v174, v88
	v_fmac_f32_e32 v46, v163, v89
	v_fmac_f32_e32 v54, v167, v89
	v_fmac_f32_e32 v62, v171, v89
	v_fmac_f32_e32 v70, v175, v89
	v_fmac_f32_e32 v46, v164, v90
	v_fmac_f32_e32 v54, v168, v90
	v_fmac_f32_e32 v62, v172, v90
	v_fmac_f32_e32 v70, v176, v90
	v_fmac_f32_e32 v46, v165, v91
	v_fmac_f32_e32 v54, v169, v91
	v_fmac_f32_e32 v62, v173, v91
	v_fmac_f32_e32 v70, v177, v91
	ds_read_b128 v[76:79], v75 offset:4096
	ds_read_b128 v[80:83], v75 offset:12288
	ds_read_b128 v[84:87], v1 offset:4096
	s_waitcnt vmcnt(12) lgkmcnt(1)
	v_fma_f32 v178, v178, v80, v76
	v_fma_f32 v179, v179, v81, v77
	v_fma_f32 v180, v180, v82, v78
	v_fma_f32 v181, v181, v83, v79
	v_max3_f32 v71, v71, |v178|, |v179|
	v_max3_f32 v71, v71, |v180|, |v181|
	v_fma_f32 v182, v182, v80, v76
	v_fma_f32 v183, v183, v81, v77
	v_fma_f32 v184, v184, v82, v78
	v_fma_f32 v185, v185, v83, v79
	v_max3_f32 v72, v72, |v182|, |v183|
	v_max3_f32 v72, v72, |v184|, |v185|
	v_fma_f32 v186, v186, v80, v76
	v_fma_f32 v187, v187, v81, v77
	v_fma_f32 v188, v188, v82, v78
	v_fma_f32 v189, v189, v83, v79
	v_max3_f32 v73, v73, |v186|, |v187|
	v_max3_f32 v73, v73, |v188|, |v189|
	v_fma_f32 v190, v190, v80, v76
	v_fma_f32 v191, v191, v81, v77
	v_fma_f32 v192, v192, v82, v78
	v_fma_f32 v193, v193, v83, v79
	v_max3_f32 v74, v74, |v190|, |v191|
	v_max3_f32 v74, v74, |v192|, |v193|
	ds_read_b128 v[88:91], v1 offset:12288
	s_waitcnt lgkmcnt(1)
	v_fmac_f32_e32 v39, v178, v84
	v_fmac_f32_e32 v47, v182, v84
	v_fmac_f32_e32 v55, v186, v84
	v_fmac_f32_e32 v63, v190, v84
	v_fmac_f32_e32 v39, v179, v85
	v_fmac_f32_e32 v47, v183, v85
	v_fmac_f32_e32 v55, v187, v85
	v_fmac_f32_e32 v63, v191, v85
	v_fmac_f32_e32 v39, v180, v86
	v_fmac_f32_e32 v47, v184, v86
	v_fmac_f32_e32 v55, v188, v86
	v_fmac_f32_e32 v63, v192, v86
	v_fmac_f32_e32 v39, v181, v87
	v_fmac_f32_e32 v47, v185, v87
	v_fmac_f32_e32 v55, v189, v87
	v_fmac_f32_e32 v63, v193, v87
	ds_read_b128 v[84:87], v1 offset:20480
	s_waitcnt lgkmcnt(1)
	v_fmac_f32_e32 v40, v178, v88
	v_fmac_f32_e32 v48, v182, v88
	v_fmac_f32_e32 v56, v186, v88
	v_fmac_f32_e32 v64, v190, v88
	v_fmac_f32_e32 v40, v179, v89
	v_fmac_f32_e32 v48, v183, v89
	v_fmac_f32_e32 v56, v187, v89
	v_fmac_f32_e32 v64, v191, v89
	v_fmac_f32_e32 v40, v180, v90
	v_fmac_f32_e32 v48, v184, v90
	v_fmac_f32_e32 v56, v188, v90
	v_fmac_f32_e32 v64, v192, v90
	v_fmac_f32_e32 v40, v181, v91
	v_fmac_f32_e32 v48, v185, v91
	v_fmac_f32_e32 v56, v189, v91
	v_fmac_f32_e32 v64, v193, v91
	ds_read_b128 v[88:91], v1 offset:28672
	s_waitcnt lgkmcnt(1)
	v_fmac_f32_e32 v41, v178, v84
	v_fmac_f32_e32 v49, v182, v84
	v_fmac_f32_e32 v57, v186, v84
	v_fmac_f32_e32 v65, v190, v84
	v_fmac_f32_e32 v41, v179, v85
	v_fmac_f32_e32 v49, v183, v85
	v_fmac_f32_e32 v57, v187, v85
	v_fmac_f32_e32 v65, v191, v85
	v_fmac_f32_e32 v41, v180, v86
	v_fmac_f32_e32 v49, v184, v86
	v_fmac_f32_e32 v57, v188, v86
	v_fmac_f32_e32 v65, v192, v86
	v_fmac_f32_e32 v41, v181, v87
	v_fmac_f32_e32 v49, v185, v87
	v_fmac_f32_e32 v57, v189, v87
	v_fmac_f32_e32 v65, v193, v87
	ds_read_b128 v[84:87], v1 offset:36864
	s_waitcnt lgkmcnt(1)
	v_fmac_f32_e32 v42, v178, v88
	v_fmac_f32_e32 v50, v182, v88
	v_fmac_f32_e32 v58, v186, v88
	v_fmac_f32_e32 v66, v190, v88
	v_fmac_f32_e32 v42, v179, v89
	v_fmac_f32_e32 v50, v183, v89
	v_fmac_f32_e32 v58, v187, v89
	v_fmac_f32_e32 v66, v191, v89
	v_fmac_f32_e32 v42, v180, v90
	v_fmac_f32_e32 v50, v184, v90
	v_fmac_f32_e32 v58, v188, v90
	v_fmac_f32_e32 v66, v192, v90
	v_fmac_f32_e32 v42, v181, v91
	v_fmac_f32_e32 v50, v185, v91
	v_fmac_f32_e32 v58, v189, v91
	v_fmac_f32_e32 v66, v193, v91
	ds_read_b128 v[88:91], v1 offset:45056
	s_waitcnt lgkmcnt(1)
	v_fmac_f32_e32 v43, v178, v84
	v_fmac_f32_e32 v51, v182, v84
	v_fmac_f32_e32 v59, v186, v84
	v_fmac_f32_e32 v67, v190, v84
	v_fmac_f32_e32 v43, v179, v85
	v_fmac_f32_e32 v51, v183, v85
	v_fmac_f32_e32 v59, v187, v85
	v_fmac_f32_e32 v67, v191, v85
	v_fmac_f32_e32 v43, v180, v86
	v_fmac_f32_e32 v51, v184, v86
	v_fmac_f32_e32 v59, v188, v86
	v_fmac_f32_e32 v67, v192, v86
	v_fmac_f32_e32 v43, v181, v87
	v_fmac_f32_e32 v51, v185, v87
	v_fmac_f32_e32 v59, v189, v87
	v_fmac_f32_e32 v67, v193, v87
	ds_read_b128 v[84:87], v1 offset:53248
	s_waitcnt lgkmcnt(1)
	v_fmac_f32_e32 v44, v178, v88
	v_fmac_f32_e32 v52, v182, v88
	v_fmac_f32_e32 v60, v186, v88
	v_fmac_f32_e32 v68, v190, v88
	v_fmac_f32_e32 v44, v179, v89
	v_fmac_f32_e32 v52, v183, v89
	v_fmac_f32_e32 v60, v187, v89
	v_fmac_f32_e32 v68, v191, v89
	v_fmac_f32_e32 v44, v180, v90
	v_fmac_f32_e32 v52, v184, v90
	v_fmac_f32_e32 v60, v188, v90
	v_fmac_f32_e32 v68, v192, v90
	v_fmac_f32_e32 v44, v181, v91
	v_fmac_f32_e32 v52, v185, v91
	v_fmac_f32_e32 v60, v189, v91
	v_fmac_f32_e32 v68, v193, v91
	ds_read_b128 v[88:91], v1 offset:61440
	s_waitcnt lgkmcnt(1)
	v_fmac_f32_e32 v45, v178, v84
	v_fmac_f32_e32 v53, v182, v84
	v_fmac_f32_e32 v61, v186, v84
	v_fmac_f32_e32 v69, v190, v84
	v_fmac_f32_e32 v45, v179, v85
	v_fmac_f32_e32 v53, v183, v85
	v_fmac_f32_e32 v61, v187, v85
	v_fmac_f32_e32 v69, v191, v85
	v_fmac_f32_e32 v45, v180, v86
	v_fmac_f32_e32 v53, v184, v86
	v_fmac_f32_e32 v61, v188, v86
	v_fmac_f32_e32 v69, v192, v86
	v_fmac_f32_e32 v45, v181, v87
	v_fmac_f32_e32 v53, v185, v87
	v_fmac_f32_e32 v61, v189, v87
	v_fmac_f32_e32 v69, v193, v87
	s_waitcnt lgkmcnt(0)
	v_fmac_f32_e32 v46, v178, v88
	v_fmac_f32_e32 v54, v182, v88
	v_fmac_f32_e32 v62, v186, v88
	v_fmac_f32_e32 v70, v190, v88
	v_fmac_f32_e32 v46, v179, v89
	v_fmac_f32_e32 v54, v183, v89
	v_fmac_f32_e32 v62, v187, v89
	v_fmac_f32_e32 v70, v191, v89
	v_fmac_f32_e32 v46, v180, v90
	v_fmac_f32_e32 v54, v184, v90
	v_fmac_f32_e32 v62, v188, v90
	v_fmac_f32_e32 v70, v192, v90
	v_fmac_f32_e32 v46, v181, v91
	v_fmac_f32_e32 v54, v185, v91
	v_fmac_f32_e32 v62, v189, v91
	v_fmac_f32_e32 v70, v193, v91
	ds_read_b128 v[76:79], v75 offset:5120
	ds_read_b128 v[80:83], v75 offset:13312
	ds_read_b128 v[84:87], v1 offset:5120
	s_waitcnt vmcnt(8) lgkmcnt(1)
	v_fma_f32 v194, v194, v80, v76
	v_fma_f32 v195, v195, v81, v77
	v_fma_f32 v196, v196, v82, v78
	v_fma_f32 v197, v197, v83, v79
	v_max3_f32 v71, v71, |v194|, |v195|
	v_max3_f32 v71, v71, |v196|, |v197|
	v_fma_f32 v198, v198, v80, v76
	v_fma_f32 v199, v199, v81, v77
	v_fma_f32 v200, v200, v82, v78
	v_fma_f32 v201, v201, v83, v79
	v_max3_f32 v72, v72, |v198|, |v199|
	v_max3_f32 v72, v72, |v200|, |v201|
	v_fma_f32 v202, v202, v80, v76
	v_fma_f32 v203, v203, v81, v77
	v_fma_f32 v204, v204, v82, v78
	v_fma_f32 v205, v205, v83, v79
	v_max3_f32 v73, v73, |v202|, |v203|
	v_max3_f32 v73, v73, |v204|, |v205|
	v_fma_f32 v206, v206, v80, v76
	v_fma_f32 v207, v207, v81, v77
	v_fma_f32 v208, v208, v82, v78
	v_fma_f32 v209, v209, v83, v79
	v_max3_f32 v74, v74, |v206|, |v207|
	v_max3_f32 v74, v74, |v208|, |v209|
	ds_read_b128 v[88:91], v1 offset:13312
	s_waitcnt lgkmcnt(1)
	v_fmac_f32_e32 v39, v194, v84
	v_fmac_f32_e32 v47, v198, v84
	v_fmac_f32_e32 v55, v202, v84
	v_fmac_f32_e32 v63, v206, v84
	v_fmac_f32_e32 v39, v195, v85
	v_fmac_f32_e32 v47, v199, v85
	v_fmac_f32_e32 v55, v203, v85
	v_fmac_f32_e32 v63, v207, v85
	v_fmac_f32_e32 v39, v196, v86
	v_fmac_f32_e32 v47, v200, v86
	v_fmac_f32_e32 v55, v204, v86
	v_fmac_f32_e32 v63, v208, v86
	v_fmac_f32_e32 v39, v197, v87
	v_fmac_f32_e32 v47, v201, v87
	v_fmac_f32_e32 v55, v205, v87
	v_fmac_f32_e32 v63, v209, v87
	ds_read_b128 v[84:87], v1 offset:21504
	s_waitcnt lgkmcnt(1)
	v_fmac_f32_e32 v40, v194, v88
	v_fmac_f32_e32 v48, v198, v88
	v_fmac_f32_e32 v56, v202, v88
	v_fmac_f32_e32 v64, v206, v88
	v_fmac_f32_e32 v40, v195, v89
	v_fmac_f32_e32 v48, v199, v89
	v_fmac_f32_e32 v56, v203, v89
	v_fmac_f32_e32 v64, v207, v89
	v_fmac_f32_e32 v40, v196, v90
	v_fmac_f32_e32 v48, v200, v90
	v_fmac_f32_e32 v56, v204, v90
	v_fmac_f32_e32 v64, v208, v90
	v_fmac_f32_e32 v40, v197, v91
	v_fmac_f32_e32 v48, v201, v91
	v_fmac_f32_e32 v56, v205, v91
	v_fmac_f32_e32 v64, v209, v91
	ds_read_b128 v[88:91], v1 offset:29696
	s_waitcnt lgkmcnt(1)
	v_fmac_f32_e32 v41, v194, v84
	v_fmac_f32_e32 v49, v198, v84
	v_fmac_f32_e32 v57, v202, v84
	v_fmac_f32_e32 v65, v206, v84
	v_fmac_f32_e32 v41, v195, v85
	v_fmac_f32_e32 v49, v199, v85
	v_fmac_f32_e32 v57, v203, v85
	v_fmac_f32_e32 v65, v207, v85
	v_fmac_f32_e32 v41, v196, v86
	v_fmac_f32_e32 v49, v200, v86
	v_fmac_f32_e32 v57, v204, v86
	v_fmac_f32_e32 v65, v208, v86
	v_fmac_f32_e32 v41, v197, v87
	v_fmac_f32_e32 v49, v201, v87
	v_fmac_f32_e32 v57, v205, v87
	v_fmac_f32_e32 v65, v209, v87
	ds_read_b128 v[84:87], v1 offset:37888
	s_waitcnt lgkmcnt(1)
	v_fmac_f32_e32 v42, v194, v88
	v_fmac_f32_e32 v50, v198, v88
	v_fmac_f32_e32 v58, v202, v88
	v_fmac_f32_e32 v66, v206, v88
	v_fmac_f32_e32 v42, v195, v89
	v_fmac_f32_e32 v50, v199, v89
	v_fmac_f32_e32 v58, v203, v89
	v_fmac_f32_e32 v66, v207, v89
	v_fmac_f32_e32 v42, v196, v90
	v_fmac_f32_e32 v50, v200, v90
	v_fmac_f32_e32 v58, v204, v90
	v_fmac_f32_e32 v66, v208, v90
	v_fmac_f32_e32 v42, v197, v91
	v_fmac_f32_e32 v50, v201, v91
	v_fmac_f32_e32 v58, v205, v91
	v_fmac_f32_e32 v66, v209, v91
	ds_read_b128 v[88:91], v1 offset:46080
	s_waitcnt lgkmcnt(1)
	v_fmac_f32_e32 v43, v194, v84
	v_fmac_f32_e32 v51, v198, v84
	v_fmac_f32_e32 v59, v202, v84
	v_fmac_f32_e32 v67, v206, v84
	v_fmac_f32_e32 v43, v195, v85
	v_fmac_f32_e32 v51, v199, v85
	v_fmac_f32_e32 v59, v203, v85
	v_fmac_f32_e32 v67, v207, v85
	v_fmac_f32_e32 v43, v196, v86
	v_fmac_f32_e32 v51, v200, v86
	v_fmac_f32_e32 v59, v204, v86
	v_fmac_f32_e32 v67, v208, v86
	v_fmac_f32_e32 v43, v197, v87
	v_fmac_f32_e32 v51, v201, v87
	v_fmac_f32_e32 v59, v205, v87
	v_fmac_f32_e32 v67, v209, v87
	ds_read_b128 v[84:87], v1 offset:54272
	s_waitcnt lgkmcnt(1)
	v_fmac_f32_e32 v44, v194, v88
	v_fmac_f32_e32 v52, v198, v88
	v_fmac_f32_e32 v60, v202, v88
	v_fmac_f32_e32 v68, v206, v88
	v_fmac_f32_e32 v44, v195, v89
	v_fmac_f32_e32 v52, v199, v89
	v_fmac_f32_e32 v60, v203, v89
	v_fmac_f32_e32 v68, v207, v89
	v_fmac_f32_e32 v44, v196, v90
	v_fmac_f32_e32 v52, v200, v90
	v_fmac_f32_e32 v60, v204, v90
	v_fmac_f32_e32 v68, v208, v90
	v_fmac_f32_e32 v44, v197, v91
	v_fmac_f32_e32 v52, v201, v91
	v_fmac_f32_e32 v60, v205, v91
	v_fmac_f32_e32 v68, v209, v91
	ds_read_b128 v[88:91], v1 offset:62464
	s_waitcnt lgkmcnt(1)
	v_fmac_f32_e32 v45, v194, v84
	v_fmac_f32_e32 v53, v198, v84
	v_fmac_f32_e32 v61, v202, v84
	v_fmac_f32_e32 v69, v206, v84
	v_fmac_f32_e32 v45, v195, v85
	v_fmac_f32_e32 v53, v199, v85
	v_fmac_f32_e32 v61, v203, v85
	v_fmac_f32_e32 v69, v207, v85
	v_fmac_f32_e32 v45, v196, v86
	v_fmac_f32_e32 v53, v200, v86
	v_fmac_f32_e32 v61, v204, v86
	v_fmac_f32_e32 v69, v208, v86
	v_fmac_f32_e32 v45, v197, v87
	v_fmac_f32_e32 v53, v201, v87
	v_fmac_f32_e32 v61, v205, v87
	v_fmac_f32_e32 v69, v209, v87
	s_waitcnt lgkmcnt(0)
	v_fmac_f32_e32 v46, v194, v88
	v_fmac_f32_e32 v54, v198, v88
	v_fmac_f32_e32 v62, v202, v88
	v_fmac_f32_e32 v70, v206, v88
	v_fmac_f32_e32 v46, v195, v89
	v_fmac_f32_e32 v54, v199, v89
	v_fmac_f32_e32 v62, v203, v89
	v_fmac_f32_e32 v70, v207, v89
	v_fmac_f32_e32 v46, v196, v90
	v_fmac_f32_e32 v54, v200, v90
	v_fmac_f32_e32 v62, v204, v90
	v_fmac_f32_e32 v70, v208, v90
	v_fmac_f32_e32 v46, v197, v91
	v_fmac_f32_e32 v54, v201, v91
	v_fmac_f32_e32 v62, v205, v91
	v_fmac_f32_e32 v70, v209, v91
	ds_read_b128 v[76:79], v75 offset:6144
	ds_read_b128 v[80:83], v75 offset:14336
	ds_read_b128 v[84:87], v1 offset:6144
	s_waitcnt vmcnt(4) lgkmcnt(1)
	v_fma_f32 v210, v210, v80, v76
	v_fma_f32 v211, v211, v81, v77
	v_fma_f32 v212, v212, v82, v78
	v_fma_f32 v213, v213, v83, v79
	v_max3_f32 v71, v71, |v210|, |v211|
	v_max3_f32 v71, v71, |v212|, |v213|
	v_fma_f32 v216, v216, v80, v76
	v_fma_f32 v217, v217, v81, v77
	v_fma_f32 v218, v218, v82, v78
	v_fma_f32 v219, v219, v83, v79
	v_max3_f32 v72, v72, |v216|, |v217|
	v_max3_f32 v72, v72, |v218|, |v219|
	v_fma_f32 v220, v220, v80, v76
	v_fma_f32 v221, v221, v81, v77
	v_fma_f32 v222, v222, v82, v78
	v_fma_f32 v223, v223, v83, v79
	v_max3_f32 v73, v73, |v220|, |v221|
	v_max3_f32 v73, v73, |v222|, |v223|
	v_fma_f32 v224, v224, v80, v76
	v_fma_f32 v225, v225, v81, v77
	v_fma_f32 v226, v226, v82, v78
	v_fma_f32 v227, v227, v83, v79
	v_max3_f32 v74, v74, |v224|, |v225|
	v_max3_f32 v74, v74, |v226|, |v227|
	ds_read_b128 v[88:91], v1 offset:14336
	s_waitcnt lgkmcnt(1)
	v_fmac_f32_e32 v39, v210, v84
	v_fmac_f32_e32 v47, v216, v84
	v_fmac_f32_e32 v55, v220, v84
	v_fmac_f32_e32 v63, v224, v84
	v_fmac_f32_e32 v39, v211, v85
	v_fmac_f32_e32 v47, v217, v85
	v_fmac_f32_e32 v55, v221, v85
	v_fmac_f32_e32 v63, v225, v85
	v_fmac_f32_e32 v39, v212, v86
	v_fmac_f32_e32 v47, v218, v86
	v_fmac_f32_e32 v55, v222, v86
	v_fmac_f32_e32 v63, v226, v86
	v_fmac_f32_e32 v39, v213, v87
	v_fmac_f32_e32 v47, v219, v87
	v_fmac_f32_e32 v55, v223, v87
	v_fmac_f32_e32 v63, v227, v87
	ds_read_b128 v[84:87], v1 offset:22528
	s_waitcnt lgkmcnt(1)
	v_fmac_f32_e32 v40, v210, v88
	v_fmac_f32_e32 v48, v216, v88
	v_fmac_f32_e32 v56, v220, v88
	v_fmac_f32_e32 v64, v224, v88
	v_fmac_f32_e32 v40, v211, v89
	v_fmac_f32_e32 v48, v217, v89
	v_fmac_f32_e32 v56, v221, v89
	v_fmac_f32_e32 v64, v225, v89
	v_fmac_f32_e32 v40, v212, v90
	v_fmac_f32_e32 v48, v218, v90
	v_fmac_f32_e32 v56, v222, v90
	v_fmac_f32_e32 v64, v226, v90
	v_fmac_f32_e32 v40, v213, v91
	v_fmac_f32_e32 v48, v219, v91
	v_fmac_f32_e32 v56, v223, v91
	v_fmac_f32_e32 v64, v227, v91
	ds_read_b128 v[88:91], v1 offset:30720
	s_waitcnt lgkmcnt(1)
	v_fmac_f32_e32 v41, v210, v84
	v_fmac_f32_e32 v49, v216, v84
	v_fmac_f32_e32 v57, v220, v84
	v_fmac_f32_e32 v65, v224, v84
	v_fmac_f32_e32 v41, v211, v85
	v_fmac_f32_e32 v49, v217, v85
	v_fmac_f32_e32 v57, v221, v85
	v_fmac_f32_e32 v65, v225, v85
	v_fmac_f32_e32 v41, v212, v86
	v_fmac_f32_e32 v49, v218, v86
	v_fmac_f32_e32 v57, v222, v86
	v_fmac_f32_e32 v65, v226, v86
	v_fmac_f32_e32 v41, v213, v87
	v_fmac_f32_e32 v49, v219, v87
	v_fmac_f32_e32 v57, v223, v87
	v_fmac_f32_e32 v65, v227, v87
	ds_read_b128 v[84:87], v1 offset:38912
	s_waitcnt lgkmcnt(1)
	v_fmac_f32_e32 v42, v210, v88
	v_fmac_f32_e32 v50, v216, v88
	v_fmac_f32_e32 v58, v220, v88
	v_fmac_f32_e32 v66, v224, v88
	v_fmac_f32_e32 v42, v211, v89
	v_fmac_f32_e32 v50, v217, v89
	v_fmac_f32_e32 v58, v221, v89
	v_fmac_f32_e32 v66, v225, v89
	v_fmac_f32_e32 v42, v212, v90
	v_fmac_f32_e32 v50, v218, v90
	v_fmac_f32_e32 v58, v222, v90
	v_fmac_f32_e32 v66, v226, v90
	v_fmac_f32_e32 v42, v213, v91
	v_fmac_f32_e32 v50, v219, v91
	v_fmac_f32_e32 v58, v223, v91
	v_fmac_f32_e32 v66, v227, v91
	ds_read_b128 v[88:91], v1 offset:47104
	s_waitcnt lgkmcnt(1)
	v_fmac_f32_e32 v43, v210, v84
	v_fmac_f32_e32 v51, v216, v84
	v_fmac_f32_e32 v59, v220, v84
	v_fmac_f32_e32 v67, v224, v84
	v_fmac_f32_e32 v43, v211, v85
	v_fmac_f32_e32 v51, v217, v85
	v_fmac_f32_e32 v59, v221, v85
	v_fmac_f32_e32 v67, v225, v85
	v_fmac_f32_e32 v43, v212, v86
	v_fmac_f32_e32 v51, v218, v86
	v_fmac_f32_e32 v59, v222, v86
	v_fmac_f32_e32 v67, v226, v86
	v_fmac_f32_e32 v43, v213, v87
	v_fmac_f32_e32 v51, v219, v87
	v_fmac_f32_e32 v59, v223, v87
	v_fmac_f32_e32 v67, v227, v87
	ds_read_b128 v[84:87], v1 offset:55296
	s_waitcnt lgkmcnt(1)
	v_fmac_f32_e32 v44, v210, v88
	v_fmac_f32_e32 v52, v216, v88
	v_fmac_f32_e32 v60, v220, v88
	v_fmac_f32_e32 v68, v224, v88
	v_fmac_f32_e32 v44, v211, v89
	v_fmac_f32_e32 v52, v217, v89
	v_fmac_f32_e32 v60, v221, v89
	v_fmac_f32_e32 v68, v225, v89
	v_fmac_f32_e32 v44, v212, v90
	v_fmac_f32_e32 v52, v218, v90
	v_fmac_f32_e32 v60, v222, v90
	v_fmac_f32_e32 v68, v226, v90
	v_fmac_f32_e32 v44, v213, v91
	v_fmac_f32_e32 v52, v219, v91
	v_fmac_f32_e32 v60, v223, v91
	v_fmac_f32_e32 v68, v227, v91
	ds_read_b128 v[88:91], v1 offset:63488
	s_waitcnt lgkmcnt(1)
	v_fmac_f32_e32 v45, v210, v84
	v_fmac_f32_e32 v53, v216, v84
	v_fmac_f32_e32 v61, v220, v84
	v_fmac_f32_e32 v69, v224, v84
	v_fmac_f32_e32 v45, v211, v85
	v_fmac_f32_e32 v53, v217, v85
	v_fmac_f32_e32 v61, v221, v85
	v_fmac_f32_e32 v69, v225, v85
	v_fmac_f32_e32 v45, v212, v86
	v_fmac_f32_e32 v53, v218, v86
	v_fmac_f32_e32 v61, v222, v86
	v_fmac_f32_e32 v69, v226, v86
	v_fmac_f32_e32 v45, v213, v87
	v_fmac_f32_e32 v53, v219, v87
	v_fmac_f32_e32 v61, v223, v87
	v_fmac_f32_e32 v69, v227, v87
	s_waitcnt lgkmcnt(0)
	v_fmac_f32_e32 v46, v210, v88
	v_fmac_f32_e32 v54, v216, v88
	v_fmac_f32_e32 v62, v220, v88
	v_fmac_f32_e32 v70, v224, v88
	v_fmac_f32_e32 v46, v211, v89
	v_fmac_f32_e32 v54, v217, v89
	v_fmac_f32_e32 v62, v221, v89
	v_fmac_f32_e32 v70, v225, v89
	v_fmac_f32_e32 v46, v212, v90
	v_fmac_f32_e32 v54, v218, v90
	v_fmac_f32_e32 v62, v222, v90
	v_fmac_f32_e32 v70, v226, v90
	v_fmac_f32_e32 v46, v213, v91
	v_fmac_f32_e32 v54, v219, v91
	v_fmac_f32_e32 v62, v223, v91
	v_fmac_f32_e32 v70, v227, v91
	ds_read_b128 v[76:79], v75 offset:7168
	ds_read_b128 v[80:83], v75 offset:15360
	ds_read_b128 v[84:87], v1 offset:7168
	s_waitcnt vmcnt(0) lgkmcnt(1)
	v_fma_f32 v228, v228, v80, v76
	v_fma_f32 v229, v229, v81, v77
	v_fma_f32 v230, v230, v82, v78
	v_fma_f32 v231, v231, v83, v79
	v_max3_f32 v71, v71, |v228|, |v229|
	v_max3_f32 v71, v71, |v230|, |v231|
	v_fma_f32 v232, v232, v80, v76
	v_fma_f32 v233, v233, v81, v77
	v_fma_f32 v234, v234, v82, v78
	v_fma_f32 v235, v235, v83, v79
	v_max3_f32 v72, v72, |v232|, |v233|
	v_max3_f32 v72, v72, |v234|, |v235|
	v_fma_f32 v236, v236, v80, v76
	v_fma_f32 v237, v237, v81, v77
	v_fma_f32 v238, v238, v82, v78
	v_fma_f32 v239, v239, v83, v79
	v_max3_f32 v73, v73, |v236|, |v237|
	v_max3_f32 v73, v73, |v238|, |v239|
	v_fma_f32 v240, v240, v80, v76
	v_fma_f32 v241, v241, v81, v77
	v_fma_f32 v242, v242, v82, v78
	v_fma_f32 v243, v243, v83, v79
	v_max3_f32 v74, v74, |v240|, |v241|
	v_max3_f32 v74, v74, |v242|, |v243|
	ds_read_b128 v[88:91], v1 offset:15360
	s_waitcnt lgkmcnt(1)
	v_fmac_f32_e32 v39, v228, v84
	v_fmac_f32_e32 v47, v232, v84
	v_fmac_f32_e32 v55, v236, v84
	v_fmac_f32_e32 v63, v240, v84
	v_fmac_f32_e32 v39, v229, v85
	v_fmac_f32_e32 v47, v233, v85
	v_fmac_f32_e32 v55, v237, v85
	v_fmac_f32_e32 v63, v241, v85
	v_fmac_f32_e32 v39, v230, v86
	v_fmac_f32_e32 v47, v234, v86
	v_fmac_f32_e32 v55, v238, v86
	v_fmac_f32_e32 v63, v242, v86
	v_fmac_f32_e32 v39, v231, v87
	v_fmac_f32_e32 v47, v235, v87
	v_fmac_f32_e32 v55, v239, v87
	v_fmac_f32_e32 v63, v243, v87
	ds_read_b128 v[84:87], v1 offset:23552
	s_waitcnt lgkmcnt(1)
	v_fmac_f32_e32 v40, v228, v88
	v_fmac_f32_e32 v48, v232, v88
	v_fmac_f32_e32 v56, v236, v88
	v_fmac_f32_e32 v64, v240, v88
	v_fmac_f32_e32 v40, v229, v89
	v_fmac_f32_e32 v48, v233, v89
	v_fmac_f32_e32 v56, v237, v89
	v_fmac_f32_e32 v64, v241, v89
	v_fmac_f32_e32 v40, v230, v90
	v_fmac_f32_e32 v48, v234, v90
	v_fmac_f32_e32 v56, v238, v90
	v_fmac_f32_e32 v64, v242, v90
	v_fmac_f32_e32 v40, v231, v91
	v_fmac_f32_e32 v48, v235, v91
	v_fmac_f32_e32 v56, v239, v91
	v_fmac_f32_e32 v64, v243, v91
	ds_read_b128 v[88:91], v1 offset:31744
	s_waitcnt lgkmcnt(1)
	v_fmac_f32_e32 v41, v228, v84
	v_fmac_f32_e32 v49, v232, v84
	v_fmac_f32_e32 v57, v236, v84
	v_fmac_f32_e32 v65, v240, v84
	v_fmac_f32_e32 v41, v229, v85
	v_fmac_f32_e32 v49, v233, v85
	v_fmac_f32_e32 v57, v237, v85
	v_fmac_f32_e32 v65, v241, v85
	v_fmac_f32_e32 v41, v230, v86
	v_fmac_f32_e32 v49, v234, v86
	v_fmac_f32_e32 v57, v238, v86
	v_fmac_f32_e32 v65, v242, v86
	v_fmac_f32_e32 v41, v231, v87
	v_fmac_f32_e32 v49, v235, v87
	v_fmac_f32_e32 v57, v239, v87
	v_fmac_f32_e32 v65, v243, v87
	ds_read_b128 v[84:87], v1 offset:39936
	s_waitcnt lgkmcnt(1)
	v_fmac_f32_e32 v42, v228, v88
	v_fmac_f32_e32 v50, v232, v88
	v_fmac_f32_e32 v58, v236, v88
	v_fmac_f32_e32 v66, v240, v88
	v_fmac_f32_e32 v42, v229, v89
	v_fmac_f32_e32 v50, v233, v89
	v_fmac_f32_e32 v58, v237, v89
	v_fmac_f32_e32 v66, v241, v89
	v_fmac_f32_e32 v42, v230, v90
	v_fmac_f32_e32 v50, v234, v90
	v_fmac_f32_e32 v58, v238, v90
	v_fmac_f32_e32 v66, v242, v90
	v_fmac_f32_e32 v42, v231, v91
	v_fmac_f32_e32 v50, v235, v91
	v_fmac_f32_e32 v58, v239, v91
	v_fmac_f32_e32 v66, v243, v91
	ds_read_b128 v[88:91], v1 offset:48128
	s_waitcnt lgkmcnt(1)
	v_fmac_f32_e32 v43, v228, v84
	v_fmac_f32_e32 v51, v232, v84
	v_fmac_f32_e32 v59, v236, v84
	v_fmac_f32_e32 v67, v240, v84
	v_fmac_f32_e32 v43, v229, v85
	v_fmac_f32_e32 v51, v233, v85
	v_fmac_f32_e32 v59, v237, v85
	v_fmac_f32_e32 v67, v241, v85
	v_fmac_f32_e32 v43, v230, v86
	v_fmac_f32_e32 v51, v234, v86
	v_fmac_f32_e32 v59, v238, v86
	v_fmac_f32_e32 v67, v242, v86
	v_fmac_f32_e32 v43, v231, v87
	v_fmac_f32_e32 v51, v235, v87
	v_fmac_f32_e32 v59, v239, v87
	v_fmac_f32_e32 v67, v243, v87
	ds_read_b128 v[84:87], v1 offset:56320
	s_waitcnt lgkmcnt(1)
	v_fmac_f32_e32 v44, v228, v88
	v_fmac_f32_e32 v52, v232, v88
	v_fmac_f32_e32 v60, v236, v88
	v_fmac_f32_e32 v68, v240, v88
	v_fmac_f32_e32 v44, v229, v89
	v_fmac_f32_e32 v52, v233, v89
	v_fmac_f32_e32 v60, v237, v89
	v_fmac_f32_e32 v68, v241, v89
	v_fmac_f32_e32 v44, v230, v90
	v_fmac_f32_e32 v52, v234, v90
	v_fmac_f32_e32 v60, v238, v90
	v_fmac_f32_e32 v68, v242, v90
	v_fmac_f32_e32 v44, v231, v91
	v_fmac_f32_e32 v52, v235, v91
	v_fmac_f32_e32 v60, v239, v91
	v_fmac_f32_e32 v68, v243, v91
	ds_read_b128 v[88:91], v1 offset:64512
	s_waitcnt lgkmcnt(1)
	v_fmac_f32_e32 v45, v228, v84
	v_fmac_f32_e32 v53, v232, v84
	v_fmac_f32_e32 v61, v236, v84
	v_fmac_f32_e32 v69, v240, v84
	v_fmac_f32_e32 v45, v229, v85
	v_fmac_f32_e32 v53, v233, v85
	v_fmac_f32_e32 v61, v237, v85
	v_fmac_f32_e32 v69, v241, v85
	v_fmac_f32_e32 v45, v230, v86
	v_fmac_f32_e32 v53, v234, v86
	v_fmac_f32_e32 v61, v238, v86
	v_fmac_f32_e32 v69, v242, v86
	v_fmac_f32_e32 v45, v231, v87
	v_fmac_f32_e32 v53, v235, v87
	v_fmac_f32_e32 v61, v239, v87
	v_fmac_f32_e32 v69, v243, v87
	s_waitcnt lgkmcnt(0)
	v_fmac_f32_e32 v46, v228, v88
	v_fmac_f32_e32 v54, v232, v88
	v_fmac_f32_e32 v62, v236, v88
	v_fmac_f32_e32 v70, v240, v88
	v_fmac_f32_e32 v46, v229, v89
	v_fmac_f32_e32 v54, v233, v89
	v_fmac_f32_e32 v62, v237, v89
	v_fmac_f32_e32 v70, v241, v89
	v_fmac_f32_e32 v46, v230, v90
	v_fmac_f32_e32 v54, v234, v90
	v_fmac_f32_e32 v62, v238, v90
	v_fmac_f32_e32 v70, v242, v90
	v_fmac_f32_e32 v46, v231, v91
	v_fmac_f32_e32 v54, v235, v91
	v_fmac_f32_e32 v62, v239, v91
	v_fmac_f32_e32 v70, v243, v91
	ds_bpermute_b32 v18, v105, v71
	ds_bpermute_b32 v19, v105, v72
	ds_bpermute_b32 v20, v105, v73
	ds_bpermute_b32 v21, v105, v74
	s_waitcnt lgkmcnt(3)
	v_max_f32_e32 v71, v71, v18
	s_waitcnt lgkmcnt(2)
	v_max_f32_e32 v72, v72, v19
	s_waitcnt lgkmcnt(1)
	v_max_f32_e32 v73, v73, v20
	s_waitcnt lgkmcnt(0)
	v_max_f32_e32 v74, v74, v21
	ds_bpermute_b32 v18, v106, v71
	ds_bpermute_b32 v19, v106, v72
	ds_bpermute_b32 v20, v106, v73
	ds_bpermute_b32 v21, v106, v74
	s_waitcnt lgkmcnt(3)
	v_max_f32_e32 v71, v71, v18
	s_waitcnt lgkmcnt(2)
	v_max_f32_e32 v72, v72, v19
	s_waitcnt lgkmcnt(1)
	v_max_f32_e32 v73, v73, v20
	s_waitcnt lgkmcnt(0)
	v_max_f32_e32 v74, v74, v21
	ds_bpermute_b32 v18, v107, v71
	ds_bpermute_b32 v19, v107, v72
	ds_bpermute_b32 v20, v107, v73
	ds_bpermute_b32 v21, v107, v74
	s_waitcnt lgkmcnt(3)
	v_max_f32_e32 v71, v71, v18
	s_waitcnt lgkmcnt(2)
	v_max_f32_e32 v72, v72, v19
	s_waitcnt lgkmcnt(1)
	v_max_f32_e32 v73, v73, v20
	s_waitcnt lgkmcnt(0)
	v_max_f32_e32 v74, v74, v21
	ds_bpermute_b32 v18, v108, v71
	ds_bpermute_b32 v19, v108, v72
	ds_bpermute_b32 v20, v108, v73
	ds_bpermute_b32 v21, v108, v74
	s_waitcnt lgkmcnt(3)
	v_max_f32_e32 v71, v71, v18
	s_waitcnt lgkmcnt(2)
	v_max_f32_e32 v72, v72, v19
	s_waitcnt lgkmcnt(1)
	v_max_f32_e32 v73, v73, v20
	s_waitcnt lgkmcnt(0)
	v_max_f32_e32 v74, v74, v21
	ds_bpermute_b32 v18, v109, v71
	ds_bpermute_b32 v19, v109, v72
	ds_bpermute_b32 v20, v109, v73
	ds_bpermute_b32 v21, v109, v74
	s_waitcnt lgkmcnt(3)
	v_max_f32_e32 v71, v71, v18
	s_waitcnt lgkmcnt(2)
	v_max_f32_e32 v72, v72, v19
	s_waitcnt lgkmcnt(1)
	v_max_f32_e32 v73, v73, v20
	s_waitcnt lgkmcnt(0)
	v_max_f32_e32 v74, v74, v21
	ds_bpermute_b32 v18, v110, v71
	ds_bpermute_b32 v19, v110, v72
	ds_bpermute_b32 v20, v110, v73
	ds_bpermute_b32 v21, v110, v74
	s_waitcnt lgkmcnt(3)
	v_max_f32_e32 v71, v71, v18
	s_waitcnt lgkmcnt(2)
	v_max_f32_e32 v72, v72, v19
	s_waitcnt lgkmcnt(1)
	v_max_f32_e32 v73, v73, v20
	s_waitcnt lgkmcnt(0)
	v_max_f32_e32 v74, v74, v21
	v_max_f32_e32 v71, s38, v71
	v_max_f32_e32 v72, s38, v72
	v_max_f32_e32 v73, s38, v73
	v_max_f32_e32 v74, s38, v74
	s_lshl_b32 s44, s8, 2
	s_add_u32 s44, s30, s44
	s_addc_u32 s45, s31, 0
	v_mul_f32_e32 v18, 0x3c010204, v71
	v_mul_f32_e32 v19, 0x3c010204, v72
	v_mul_f32_e32 v20, 0x3c010204, v73
	v_mul_f32_e32 v21, 0x3c010204, v74
	s_and_saveexec_b64 s[16:17], s[0:1]
	global_store_dword v29, v18, s[44:45]
	global_store_dword v29, v19, s[44:45] offset:4
	global_store_dword v29, v20, s[44:45] offset:8
	global_store_dword v29, v21, s[44:45] offset:12
	s_or_b64 exec, exec, s[16:17]
	v_div_scale_f32 v92, s[22:23], v71, v71, s39
	v_rcp_f32_e32 v93, v92
	v_div_scale_f32 v94, vcc, s39, v71, s39
	v_fma_f32 v95, -v92, v93, 1.0
	v_fmac_f32_e32 v93, v95, v93
	v_mul_f32_e32 v95, v94, v93
	v_fma_f32 v96, -v92, v95, v94
	v_fmac_f32_e32 v95, v96, v93
	v_fma_f32 v92, -v92, v95, v94
	v_div_fmas_f32 v92, v92, v93, v95
	v_div_fixup_f32 v71, v92, v71, s39
	v_div_scale_f32 v92, s[22:23], v72, v72, s39
	v_rcp_f32_e32 v93, v92
	v_div_scale_f32 v94, vcc, s39, v72, s39
	v_fma_f32 v95, -v92, v93, 1.0
	v_fmac_f32_e32 v93, v95, v93
	v_mul_f32_e32 v95, v94, v93
	v_fma_f32 v96, -v92, v95, v94
	v_fmac_f32_e32 v95, v96, v93
	v_fma_f32 v92, -v92, v95, v94
	v_div_fmas_f32 v92, v92, v93, v95
	v_div_fixup_f32 v72, v92, v72, s39
	v_div_scale_f32 v92, s[22:23], v73, v73, s39
	v_rcp_f32_e32 v93, v92
	v_div_scale_f32 v94, vcc, s39, v73, s39
	v_fma_f32 v95, -v92, v93, 1.0
	v_fmac_f32_e32 v93, v95, v93
	v_mul_f32_e32 v95, v94, v93
	v_fma_f32 v96, -v92, v95, v94
	v_fmac_f32_e32 v95, v96, v93
	v_fma_f32 v92, -v92, v95, v94
	v_div_fmas_f32 v92, v92, v93, v95
	v_div_fixup_f32 v73, v92, v73, s39
	v_div_scale_f32 v92, s[22:23], v74, v74, s39
	v_rcp_f32_e32 v93, v92
	v_div_scale_f32 v94, vcc, s39, v74, s39
	v_fma_f32 v95, -v92, v93, 1.0
	v_fmac_f32_e32 v93, v95, v93
	v_mul_f32_e32 v95, v94, v93
	v_fma_f32 v96, -v92, v95, v94
	v_fmac_f32_e32 v95, v96, v93
	v_fma_f32 v92, -v92, v95, v94
	v_div_fmas_f32 v92, v92, v93, v95
	v_div_fixup_f32 v74, v92, v74, s39
	s_lshl_b32 s44, s92, 11
	s_mov_b32 s45, 0
	v_lshl_add_u64 v[2:3], v[36:37], 0, s[44:45]
	s_mov_b64 s[44:45], 0x1000
	v_lshl_add_u64 v[4:5], v[2:3], 0, s[44:45]
	v_fmaak_f32 v97, v114, v71, 0x4b400000
	v_fmaak_f32 v98, v115, v71, 0x4b400000
	v_fmaak_f32 v99, v116, v71, 0x4b400000
	v_fmaak_f32 v100, v117, v71, 0x4b400000
	v_med3_f32 v97, v97, s40, v112
	v_med3_f32 v98, v98, s40, v112
	v_med3_f32 v99, v99, s40, v112
	v_med3_f32 v100, v100, s40, v112
	v_perm_b32 v97, v98, v97, s41
	v_perm_b32 v99, v100, v99, s41
	v_perm_b32 v101, v99, v97, s42
	global_store_dword v[2:3], v101, off offset:0 sc1
	v_fmaak_f32 v97, v130, v71, 0x4b400000
	v_fmaak_f32 v98, v131, v71, 0x4b400000
	v_fmaak_f32 v99, v132, v71, 0x4b400000
	v_fmaak_f32 v100, v133, v71, 0x4b400000
	v_med3_f32 v97, v97, s40, v112
	v_med3_f32 v98, v98, s40, v112
	v_med3_f32 v99, v99, s40, v112
	v_med3_f32 v100, v100, s40, v112
	v_perm_b32 v97, v98, v97, s41
	v_perm_b32 v99, v100, v99, s41
	v_perm_b32 v102, v99, v97, s42
	global_store_dword v[2:3], v102, off offset:256 sc1
	v_fmaak_f32 v97, v146, v71, 0x4b400000
	v_fmaak_f32 v98, v147, v71, 0x4b400000
	v_fmaak_f32 v99, v148, v71, 0x4b400000
	v_fmaak_f32 v100, v149, v71, 0x4b400000
	v_med3_f32 v97, v97, s40, v112
	v_med3_f32 v98, v98, s40, v112
	v_med3_f32 v99, v99, s40, v112
	v_med3_f32 v100, v100, s40, v112
	v_perm_b32 v97, v98, v97, s41
	v_perm_b32 v99, v100, v99, s41
	v_perm_b32 v101, v99, v97, s42
	global_store_dword v[2:3], v101, off offset:512 sc1
	v_fmaak_f32 v97, v162, v71, 0x4b400000
	v_fmaak_f32 v98, v163, v71, 0x4b400000
	v_fmaak_f32 v99, v164, v71, 0x4b400000
	v_fmaak_f32 v100, v165, v71, 0x4b400000
	v_med3_f32 v97, v97, s40, v112
	v_med3_f32 v98, v98, s40, v112
	v_med3_f32 v99, v99, s40, v112
	v_med3_f32 v100, v100, s40, v112
	v_perm_b32 v97, v98, v97, s41
	v_perm_b32 v99, v100, v99, s41
	v_perm_b32 v102, v99, v97, s42
	global_store_dword v[2:3], v102, off offset:768 sc1
	v_fmaak_f32 v97, v178, v71, 0x4b400000
	v_fmaak_f32 v98, v179, v71, 0x4b400000
	v_fmaak_f32 v99, v180, v71, 0x4b400000
	v_fmaak_f32 v100, v181, v71, 0x4b400000
	v_med3_f32 v97, v97, s40, v112
	v_med3_f32 v98, v98, s40, v112
	v_med3_f32 v99, v99, s40, v112
	v_med3_f32 v100, v100, s40, v112
	v_perm_b32 v97, v98, v97, s41
	v_perm_b32 v99, v100, v99, s41
	v_perm_b32 v101, v99, v97, s42
	global_store_dword v[2:3], v101, off offset:1024 sc1
	v_fmaak_f32 v97, v194, v71, 0x4b400000
	v_fmaak_f32 v98, v195, v71, 0x4b400000
	v_fmaak_f32 v99, v196, v71, 0x4b400000
	v_fmaak_f32 v100, v197, v71, 0x4b400000
	v_med3_f32 v97, v97, s40, v112
	v_med3_f32 v98, v98, s40, v112
	v_med3_f32 v99, v99, s40, v112
	v_med3_f32 v100, v100, s40, v112
	v_perm_b32 v97, v98, v97, s41
	v_perm_b32 v99, v100, v99, s41
	v_perm_b32 v102, v99, v97, s42
	global_store_dword v[2:3], v102, off offset:1280 sc1
	v_fmaak_f32 v97, v210, v71, 0x4b400000
	v_fmaak_f32 v98, v211, v71, 0x4b400000
	v_fmaak_f32 v99, v212, v71, 0x4b400000
	v_fmaak_f32 v100, v213, v71, 0x4b400000
	v_med3_f32 v97, v97, s40, v112
	v_med3_f32 v98, v98, s40, v112
	v_med3_f32 v99, v99, s40, v112
	v_med3_f32 v100, v100, s40, v112
	v_perm_b32 v97, v98, v97, s41
	v_perm_b32 v99, v100, v99, s41
	v_perm_b32 v101, v99, v97, s42
	global_store_dword v[2:3], v101, off offset:1536 sc1
	v_fmaak_f32 v97, v228, v71, 0x4b400000
	v_fmaak_f32 v98, v229, v71, 0x4b400000
	v_fmaak_f32 v99, v230, v71, 0x4b400000
	v_fmaak_f32 v100, v231, v71, 0x4b400000
	v_med3_f32 v97, v97, s40, v112
	v_med3_f32 v98, v98, s40, v112
	v_med3_f32 v99, v99, s40, v112
	v_med3_f32 v100, v100, s40, v112
	v_perm_b32 v97, v98, v97, s41
	v_perm_b32 v99, v100, v99, s41
	v_perm_b32 v102, v99, v97, s42
	global_store_dword v[2:3], v102, off offset:1792 sc1
	v_fmaak_f32 v97, v118, v72, 0x4b400000
	v_fmaak_f32 v98, v119, v72, 0x4b400000
	v_fmaak_f32 v99, v120, v72, 0x4b400000
	v_fmaak_f32 v100, v121, v72, 0x4b400000
	v_med3_f32 v97, v97, s40, v112
	v_med3_f32 v98, v98, s40, v112
	v_med3_f32 v99, v99, s40, v112
	v_med3_f32 v100, v100, s40, v112
	v_perm_b32 v97, v98, v97, s41
	v_perm_b32 v99, v100, v99, s41
	v_perm_b32 v101, v99, v97, s42
	global_store_dword v[2:3], v101, off offset:2048 sc1
	v_fmaak_f32 v97, v134, v72, 0x4b400000
	v_fmaak_f32 v98, v135, v72, 0x4b400000
	v_fmaak_f32 v99, v136, v72, 0x4b400000
	v_fmaak_f32 v100, v137, v72, 0x4b400000
	v_med3_f32 v97, v97, s40, v112
	v_med3_f32 v98, v98, s40, v112
	v_med3_f32 v99, v99, s40, v112
	v_med3_f32 v100, v100, s40, v112
	v_perm_b32 v97, v98, v97, s41
	v_perm_b32 v99, v100, v99, s41
	v_perm_b32 v102, v99, v97, s42
	global_store_dword v[2:3], v102, off offset:2304 sc1
	v_fmaak_f32 v97, v150, v72, 0x4b400000
	v_fmaak_f32 v98, v151, v72, 0x4b400000
	v_fmaak_f32 v99, v152, v72, 0x4b400000
	v_fmaak_f32 v100, v153, v72, 0x4b400000
	v_med3_f32 v97, v97, s40, v112
	v_med3_f32 v98, v98, s40, v112
	v_med3_f32 v99, v99, s40, v112
	v_med3_f32 v100, v100, s40, v112
	v_perm_b32 v97, v98, v97, s41
	v_perm_b32 v99, v100, v99, s41
	v_perm_b32 v101, v99, v97, s42
	global_store_dword v[2:3], v101, off offset:2560 sc1
	v_fmaak_f32 v97, v166, v72, 0x4b400000
	v_fmaak_f32 v98, v167, v72, 0x4b400000
	v_fmaak_f32 v99, v168, v72, 0x4b400000
	v_fmaak_f32 v100, v169, v72, 0x4b400000
	v_med3_f32 v97, v97, s40, v112
	v_med3_f32 v98, v98, s40, v112
	v_med3_f32 v99, v99, s40, v112
	v_med3_f32 v100, v100, s40, v112
	v_perm_b32 v97, v98, v97, s41
	v_perm_b32 v99, v100, v99, s41
	v_perm_b32 v102, v99, v97, s42
	global_store_dword v[2:3], v102, off offset:2816 sc1
	v_fmaak_f32 v97, v182, v72, 0x4b400000
	v_fmaak_f32 v98, v183, v72, 0x4b400000
	v_fmaak_f32 v99, v184, v72, 0x4b400000
	v_fmaak_f32 v100, v185, v72, 0x4b400000
	v_med3_f32 v97, v97, s40, v112
	v_med3_f32 v98, v98, s40, v112
	v_med3_f32 v99, v99, s40, v112
	v_med3_f32 v100, v100, s40, v112
	v_perm_b32 v97, v98, v97, s41
	v_perm_b32 v99, v100, v99, s41
	v_perm_b32 v101, v99, v97, s42
	global_store_dword v[2:3], v101, off offset:3072 sc1
	v_fmaak_f32 v97, v198, v72, 0x4b400000
	v_fmaak_f32 v98, v199, v72, 0x4b400000
	v_fmaak_f32 v99, v200, v72, 0x4b400000
	v_fmaak_f32 v100, v201, v72, 0x4b400000
	v_med3_f32 v97, v97, s40, v112
	v_med3_f32 v98, v98, s40, v112
	v_med3_f32 v99, v99, s40, v112
	v_med3_f32 v100, v100, s40, v112
	v_perm_b32 v97, v98, v97, s41
	v_perm_b32 v99, v100, v99, s41
	v_perm_b32 v102, v99, v97, s42
	global_store_dword v[2:3], v102, off offset:3328 sc1
	v_fmaak_f32 v97, v216, v72, 0x4b400000
	v_fmaak_f32 v98, v217, v72, 0x4b400000
	v_fmaak_f32 v99, v218, v72, 0x4b400000
	v_fmaak_f32 v100, v219, v72, 0x4b400000
	v_med3_f32 v97, v97, s40, v112
	v_med3_f32 v98, v98, s40, v112
	v_med3_f32 v99, v99, s40, v112
	v_med3_f32 v100, v100, s40, v112
	v_perm_b32 v97, v98, v97, s41
	v_perm_b32 v99, v100, v99, s41
	v_perm_b32 v101, v99, v97, s42
	global_store_dword v[2:3], v101, off offset:3584 sc1
	v_fmaak_f32 v97, v232, v72, 0x4b400000
	v_fmaak_f32 v98, v233, v72, 0x4b400000
	v_fmaak_f32 v99, v234, v72, 0x4b400000
	v_fmaak_f32 v100, v235, v72, 0x4b400000
	v_med3_f32 v97, v97, s40, v112
	v_med3_f32 v98, v98, s40, v112
	v_med3_f32 v99, v99, s40, v112
	v_med3_f32 v100, v100, s40, v112
	v_perm_b32 v97, v98, v97, s41
	v_perm_b32 v99, v100, v99, s41
	v_perm_b32 v102, v99, v97, s42
	global_store_dword v[2:3], v102, off offset:3840 sc1
	v_fmaak_f32 v97, v122, v73, 0x4b400000
	v_fmaak_f32 v98, v123, v73, 0x4b400000
	v_fmaak_f32 v99, v124, v73, 0x4b400000
	v_fmaak_f32 v100, v125, v73, 0x4b400000
	v_med3_f32 v97, v97, s40, v112
	v_med3_f32 v98, v98, s40, v112
	v_med3_f32 v99, v99, s40, v112
	v_med3_f32 v100, v100, s40, v112
	v_perm_b32 v97, v98, v97, s41
	v_perm_b32 v99, v100, v99, s41
	v_perm_b32 v101, v99, v97, s42
	global_store_dword v[4:5], v101, off offset:0 sc1
	v_fmaak_f32 v97, v138, v73, 0x4b400000
	v_fmaak_f32 v98, v139, v73, 0x4b400000
	v_fmaak_f32 v99, v140, v73, 0x4b400000
	v_fmaak_f32 v100, v141, v73, 0x4b400000
	v_med3_f32 v97, v97, s40, v112
	v_med3_f32 v98, v98, s40, v112
	v_med3_f32 v99, v99, s40, v112
	v_med3_f32 v100, v100, s40, v112
	v_perm_b32 v97, v98, v97, s41
	v_perm_b32 v99, v100, v99, s41
	v_perm_b32 v102, v99, v97, s42
	global_store_dword v[4:5], v102, off offset:256 sc1
	v_fmaak_f32 v97, v154, v73, 0x4b400000
	v_fmaak_f32 v98, v155, v73, 0x4b400000
	v_fmaak_f32 v99, v156, v73, 0x4b400000
	v_fmaak_f32 v100, v157, v73, 0x4b400000
	v_med3_f32 v97, v97, s40, v112
	v_med3_f32 v98, v98, s40, v112
	v_med3_f32 v99, v99, s40, v112
	v_med3_f32 v100, v100, s40, v112
	v_perm_b32 v97, v98, v97, s41
	v_perm_b32 v99, v100, v99, s41
	v_perm_b32 v101, v99, v97, s42
	global_store_dword v[4:5], v101, off offset:512 sc1
	v_fmaak_f32 v97, v170, v73, 0x4b400000
	v_fmaak_f32 v98, v171, v73, 0x4b400000
	v_fmaak_f32 v99, v172, v73, 0x4b400000
	v_fmaak_f32 v100, v173, v73, 0x4b400000
	v_med3_f32 v97, v97, s40, v112
	v_med3_f32 v98, v98, s40, v112
	v_med3_f32 v99, v99, s40, v112
	v_med3_f32 v100, v100, s40, v112
	v_perm_b32 v97, v98, v97, s41
	v_perm_b32 v99, v100, v99, s41
	v_perm_b32 v102, v99, v97, s42
	global_store_dword v[4:5], v102, off offset:768 sc1
	v_fmaak_f32 v97, v186, v73, 0x4b400000
	v_fmaak_f32 v98, v187, v73, 0x4b400000
	v_fmaak_f32 v99, v188, v73, 0x4b400000
	v_fmaak_f32 v100, v189, v73, 0x4b400000
	v_med3_f32 v97, v97, s40, v112
	v_med3_f32 v98, v98, s40, v112
	v_med3_f32 v99, v99, s40, v112
	v_med3_f32 v100, v100, s40, v112
	v_perm_b32 v97, v98, v97, s41
	v_perm_b32 v99, v100, v99, s41
	v_perm_b32 v101, v99, v97, s42
	global_store_dword v[4:5], v101, off offset:1024 sc1
	v_fmaak_f32 v97, v202, v73, 0x4b400000
	v_fmaak_f32 v98, v203, v73, 0x4b400000
	v_fmaak_f32 v99, v204, v73, 0x4b400000
	v_fmaak_f32 v100, v205, v73, 0x4b400000
	v_med3_f32 v97, v97, s40, v112
	v_med3_f32 v98, v98, s40, v112
	v_med3_f32 v99, v99, s40, v112
	v_med3_f32 v100, v100, s40, v112
	v_perm_b32 v97, v98, v97, s41
	v_perm_b32 v99, v100, v99, s41
	v_perm_b32 v102, v99, v97, s42
	global_store_dword v[4:5], v102, off offset:1280 sc1
	v_fmaak_f32 v97, v220, v73, 0x4b400000
	v_fmaak_f32 v98, v221, v73, 0x4b400000
	v_fmaak_f32 v99, v222, v73, 0x4b400000
	v_fmaak_f32 v100, v223, v73, 0x4b400000
	v_med3_f32 v97, v97, s40, v112
	v_med3_f32 v98, v98, s40, v112
	v_med3_f32 v99, v99, s40, v112
	v_med3_f32 v100, v100, s40, v112
	v_perm_b32 v97, v98, v97, s41
	v_perm_b32 v99, v100, v99, s41
	v_perm_b32 v101, v99, v97, s42
	global_store_dword v[4:5], v101, off offset:1536 sc1
	v_fmaak_f32 v97, v236, v73, 0x4b400000
	v_fmaak_f32 v98, v237, v73, 0x4b400000
	v_fmaak_f32 v99, v238, v73, 0x4b400000
	v_fmaak_f32 v100, v239, v73, 0x4b400000
	v_med3_f32 v97, v97, s40, v112
	v_med3_f32 v98, v98, s40, v112
	v_med3_f32 v99, v99, s40, v112
	v_med3_f32 v100, v100, s40, v112
	v_perm_b32 v97, v98, v97, s41
	v_perm_b32 v99, v100, v99, s41
	v_perm_b32 v102, v99, v97, s42
	global_store_dword v[4:5], v102, off offset:1792 sc1
	v_fmaak_f32 v97, v126, v74, 0x4b400000
	v_fmaak_f32 v98, v127, v74, 0x4b400000
	v_fmaak_f32 v99, v128, v74, 0x4b400000
	v_fmaak_f32 v100, v129, v74, 0x4b400000
	v_med3_f32 v97, v97, s40, v112
	v_med3_f32 v98, v98, s40, v112
	v_med3_f32 v99, v99, s40, v112
	v_med3_f32 v100, v100, s40, v112
	v_perm_b32 v97, v98, v97, s41
	v_perm_b32 v99, v100, v99, s41
	v_perm_b32 v101, v99, v97, s42
	global_store_dword v[4:5], v101, off offset:2048 sc1
	v_fmaak_f32 v97, v142, v74, 0x4b400000
	v_fmaak_f32 v98, v143, v74, 0x4b400000
	v_fmaak_f32 v99, v144, v74, 0x4b400000
	v_fmaak_f32 v100, v145, v74, 0x4b400000
	v_med3_f32 v97, v97, s40, v112
	v_med3_f32 v98, v98, s40, v112
	v_med3_f32 v99, v99, s40, v112
	v_med3_f32 v100, v100, s40, v112
	v_perm_b32 v97, v98, v97, s41
	v_perm_b32 v99, v100, v99, s41
	v_perm_b32 v102, v99, v97, s42
	global_store_dword v[4:5], v102, off offset:2304 sc1
	v_fmaak_f32 v97, v158, v74, 0x4b400000
	v_fmaak_f32 v98, v159, v74, 0x4b400000
	v_fmaak_f32 v99, v160, v74, 0x4b400000
	v_fmaak_f32 v100, v161, v74, 0x4b400000
	v_med3_f32 v97, v97, s40, v112
	v_med3_f32 v98, v98, s40, v112
	v_med3_f32 v99, v99, s40, v112
	v_med3_f32 v100, v100, s40, v112
	v_perm_b32 v97, v98, v97, s41
	v_perm_b32 v99, v100, v99, s41
	v_perm_b32 v101, v99, v97, s42
	global_store_dword v[4:5], v101, off offset:2560 sc1
	v_fmaak_f32 v97, v174, v74, 0x4b400000
	v_fmaak_f32 v98, v175, v74, 0x4b400000
	v_fmaak_f32 v99, v176, v74, 0x4b400000
	v_fmaak_f32 v100, v177, v74, 0x4b400000
	v_med3_f32 v97, v97, s40, v112
	v_med3_f32 v98, v98, s40, v112
	v_med3_f32 v99, v99, s40, v112
	v_med3_f32 v100, v100, s40, v112
	v_perm_b32 v97, v98, v97, s41
	v_perm_b32 v99, v100, v99, s41
	v_perm_b32 v102, v99, v97, s42
	global_store_dword v[4:5], v102, off offset:2816 sc1
	v_fmaak_f32 v97, v190, v74, 0x4b400000
	v_fmaak_f32 v98, v191, v74, 0x4b400000
	v_fmaak_f32 v99, v192, v74, 0x4b400000
	v_fmaak_f32 v100, v193, v74, 0x4b400000
	v_med3_f32 v97, v97, s40, v112
	v_med3_f32 v98, v98, s40, v112
	v_med3_f32 v99, v99, s40, v112
	v_med3_f32 v100, v100, s40, v112
	v_perm_b32 v97, v98, v97, s41
	v_perm_b32 v99, v100, v99, s41
	v_perm_b32 v101, v99, v97, s42
	global_store_dword v[4:5], v101, off offset:3072 sc1
	v_fmaak_f32 v97, v206, v74, 0x4b400000
	v_fmaak_f32 v98, v207, v74, 0x4b400000
	v_fmaak_f32 v99, v208, v74, 0x4b400000
	v_fmaak_f32 v100, v209, v74, 0x4b400000
	v_med3_f32 v97, v97, s40, v112
	v_med3_f32 v98, v98, s40, v112
	v_med3_f32 v99, v99, s40, v112
	v_med3_f32 v100, v100, s40, v112
	v_perm_b32 v97, v98, v97, s41
	v_perm_b32 v99, v100, v99, s41
	v_perm_b32 v102, v99, v97, s42
	global_store_dword v[4:5], v102, off offset:3328 sc1
	v_fmaak_f32 v97, v224, v74, 0x4b400000
	v_fmaak_f32 v98, v225, v74, 0x4b400000
	v_fmaak_f32 v99, v226, v74, 0x4b400000
	v_fmaak_f32 v100, v227, v74, 0x4b400000
	v_med3_f32 v97, v97, s40, v112
	v_med3_f32 v98, v98, s40, v112
	v_med3_f32 v99, v99, s40, v112
	v_med3_f32 v100, v100, s40, v112
	v_perm_b32 v97, v98, v97, s41
	v_perm_b32 v99, v100, v99, s41
	v_perm_b32 v101, v99, v97, s42
	global_store_dword v[4:5], v101, off offset:3584 sc1
	v_fmaak_f32 v97, v240, v74, 0x4b400000
	v_fmaak_f32 v98, v241, v74, 0x4b400000
	v_fmaak_f32 v99, v242, v74, 0x4b400000
	v_fmaak_f32 v100, v243, v74, 0x4b400000
	v_med3_f32 v97, v97, s40, v112
	v_med3_f32 v98, v98, s40, v112
	v_med3_f32 v99, v99, s40, v112
	v_med3_f32 v100, v100, s40, v112
	v_perm_b32 v97, v98, v97, s41
	v_perm_b32 v99, v100, v99, s41
	v_perm_b32 v102, v99, v97, s42
	global_store_dword v[4:5], v102, off offset:3840 sc1
	v_lshrrev_b32_e32 v2, 4, v214
	v_and_b32_e32 v18, 16, v214
	v_cmp_ne_u32_e64 s[52:53], 0, v18
	v_and_b32_e32 v18, 8, v214
	v_cmp_ne_u32_e64 s[54:55], 0, v18
	v_and_b32_e32 v18, 4, v214
	v_cmp_ne_u32_e64 s[56:57], 0, v18
	v_and_b32_e32 v18, 2, v214
	v_cmp_ne_u32_e64 s[58:59], 0, v18
	v_and_b32_e32 v18, 1, v214
	v_cmp_ne_u32_e64 s[60:61], 0, v18
	v_cndmask_b32_e64 v244, v55, v39, s[52:53]
	v_cndmask_b32_e64 v39, v39, v55, s[52:53]
	ds_bpermute_b32 v244, v109, v244
	v_cndmask_b32_e64 v245, v56, v40, s[52:53]
	v_cndmask_b32_e64 v40, v40, v56, s[52:53]
	ds_bpermute_b32 v245, v109, v245
	v_cndmask_b32_e64 v246, v57, v41, s[52:53]
	v_cndmask_b32_e64 v41, v41, v57, s[52:53]
	ds_bpermute_b32 v246, v109, v246
	v_cndmask_b32_e64 v247, v58, v42, s[52:53]
	v_cndmask_b32_e64 v42, v42, v58, s[52:53]
	ds_bpermute_b32 v247, v109, v247
	s_waitcnt lgkmcnt(3)
	v_add_f32_e32 v39, v39, v244
	s_waitcnt lgkmcnt(2)
	v_add_f32_e32 v40, v40, v245
	s_waitcnt lgkmcnt(1)
	v_add_f32_e32 v41, v41, v246
	s_waitcnt lgkmcnt(0)
	v_add_f32_e32 v42, v42, v247
	v_cndmask_b32_e64 v244, v59, v43, s[52:53]
	v_cndmask_b32_e64 v43, v43, v59, s[52:53]
	ds_bpermute_b32 v244, v109, v244
	v_cndmask_b32_e64 v245, v60, v44, s[52:53]
	v_cndmask_b32_e64 v44, v44, v60, s[52:53]
	ds_bpermute_b32 v245, v109, v245
	v_cndmask_b32_e64 v246, v61, v45, s[52:53]
	v_cndmask_b32_e64 v45, v45, v61, s[52:53]
	ds_bpermute_b32 v246, v109, v246
	v_cndmask_b32_e64 v247, v62, v46, s[52:53]
	v_cndmask_b32_e64 v46, v46, v62, s[52:53]
	ds_bpermute_b32 v247, v109, v247
	s_waitcnt lgkmcnt(3)
	v_add_f32_e32 v43, v43, v244
	s_waitcnt lgkmcnt(2)
	v_add_f32_e32 v44, v44, v245
	s_waitcnt lgkmcnt(1)
	v_add_f32_e32 v45, v45, v246
	s_waitcnt lgkmcnt(0)
	v_add_f32_e32 v46, v46, v247
	v_cndmask_b32_e64 v244, v63, v47, s[52:53]
	v_cndmask_b32_e64 v47, v47, v63, s[52:53]
	ds_bpermute_b32 v244, v109, v244
	v_cndmask_b32_e64 v245, v64, v48, s[52:53]
	v_cndmask_b32_e64 v48, v48, v64, s[52:53]
	ds_bpermute_b32 v245, v109, v245
	v_cndmask_b32_e64 v246, v65, v49, s[52:53]
	v_cndmask_b32_e64 v49, v49, v65, s[52:53]
	ds_bpermute_b32 v246, v109, v246
	v_cndmask_b32_e64 v247, v66, v50, s[52:53]
	v_cndmask_b32_e64 v50, v50, v66, s[52:53]
	ds_bpermute_b32 v247, v109, v247
	s_waitcnt lgkmcnt(3)
	v_add_f32_e32 v47, v47, v244
	s_waitcnt lgkmcnt(2)
	v_add_f32_e32 v48, v48, v245
	s_waitcnt lgkmcnt(1)
	v_add_f32_e32 v49, v49, v246
	s_waitcnt lgkmcnt(0)
	v_add_f32_e32 v50, v50, v247
	v_cndmask_b32_e64 v244, v67, v51, s[52:53]
	v_cndmask_b32_e64 v51, v51, v67, s[52:53]
	ds_bpermute_b32 v244, v109, v244
	v_cndmask_b32_e64 v245, v68, v52, s[52:53]
	v_cndmask_b32_e64 v52, v52, v68, s[52:53]
	ds_bpermute_b32 v245, v109, v245
	v_cndmask_b32_e64 v246, v69, v53, s[52:53]
	v_cndmask_b32_e64 v53, v53, v69, s[52:53]
	ds_bpermute_b32 v246, v109, v246
	v_cndmask_b32_e64 v247, v70, v54, s[52:53]
	v_cndmask_b32_e64 v54, v54, v70, s[52:53]
	ds_bpermute_b32 v247, v109, v247
	s_waitcnt lgkmcnt(3)
	v_add_f32_e32 v51, v51, v244
	s_waitcnt lgkmcnt(2)
	v_add_f32_e32 v52, v52, v245
	s_waitcnt lgkmcnt(1)
	v_add_f32_e32 v53, v53, v246
	s_waitcnt lgkmcnt(0)
	v_add_f32_e32 v54, v54, v247
	v_cndmask_b32_e64 v244, v47, v39, s[54:55]
	v_cndmask_b32_e64 v39, v39, v47, s[54:55]
	ds_bpermute_b32 v244, v108, v244
	v_cndmask_b32_e64 v245, v48, v40, s[54:55]
	v_cndmask_b32_e64 v40, v40, v48, s[54:55]
	ds_bpermute_b32 v245, v108, v245
	v_cndmask_b32_e64 v246, v49, v41, s[54:55]
	v_cndmask_b32_e64 v41, v41, v49, s[54:55]
	ds_bpermute_b32 v246, v108, v246
	v_cndmask_b32_e64 v247, v50, v42, s[54:55]
	v_cndmask_b32_e64 v42, v42, v50, s[54:55]
	ds_bpermute_b32 v247, v108, v247
	s_waitcnt lgkmcnt(3)
	v_add_f32_e32 v39, v39, v244
	s_waitcnt lgkmcnt(2)
	v_add_f32_e32 v40, v40, v245
	s_waitcnt lgkmcnt(1)
	v_add_f32_e32 v41, v41, v246
	s_waitcnt lgkmcnt(0)
	v_add_f32_e32 v42, v42, v247
	v_cndmask_b32_e64 v244, v51, v43, s[54:55]
	v_cndmask_b32_e64 v43, v43, v51, s[54:55]
	ds_bpermute_b32 v244, v108, v244
	v_cndmask_b32_e64 v245, v52, v44, s[54:55]
	v_cndmask_b32_e64 v44, v44, v52, s[54:55]
	ds_bpermute_b32 v245, v108, v245
	v_cndmask_b32_e64 v246, v53, v45, s[54:55]
	v_cndmask_b32_e64 v45, v45, v53, s[54:55]
	ds_bpermute_b32 v246, v108, v246
	v_cndmask_b32_e64 v247, v54, v46, s[54:55]
	v_cndmask_b32_e64 v46, v46, v54, s[54:55]
	ds_bpermute_b32 v247, v108, v247
	s_waitcnt lgkmcnt(3)
	v_add_f32_e32 v43, v43, v244
	s_waitcnt lgkmcnt(2)
	v_add_f32_e32 v44, v44, v245
	s_waitcnt lgkmcnt(1)
	v_add_f32_e32 v45, v45, v246
	s_waitcnt lgkmcnt(0)
	v_add_f32_e32 v46, v46, v247
	v_cndmask_b32_e64 v244, v43, v39, s[56:57]
	v_cndmask_b32_e64 v39, v39, v43, s[56:57]
	ds_bpermute_b32 v244, v107, v244
	v_cndmask_b32_e64 v245, v44, v40, s[56:57]
	v_cndmask_b32_e64 v40, v40, v44, s[56:57]
	ds_bpermute_b32 v245, v107, v245
	v_cndmask_b32_e64 v246, v45, v41, s[56:57]
	v_cndmask_b32_e64 v41, v41, v45, s[56:57]
	ds_bpermute_b32 v246, v107, v246
	v_cndmask_b32_e64 v247, v46, v42, s[56:57]
	v_cndmask_b32_e64 v42, v42, v46, s[56:57]
	ds_bpermute_b32 v247, v107, v247
	s_waitcnt lgkmcnt(3)
	v_add_f32_e32 v39, v39, v244
	s_waitcnt lgkmcnt(2)
	v_add_f32_e32 v40, v40, v245
	s_waitcnt lgkmcnt(1)
	v_add_f32_e32 v41, v41, v246
	s_waitcnt lgkmcnt(0)
	v_add_f32_e32 v42, v42, v247
	v_cndmask_b32_e64 v244, v41, v39, s[58:59]
	v_cndmask_b32_e64 v39, v39, v41, s[58:59]
	ds_bpermute_b32 v244, v106, v244
	v_cndmask_b32_e64 v245, v42, v40, s[58:59]
	v_cndmask_b32_e64 v40, v40, v42, s[58:59]
	ds_bpermute_b32 v245, v106, v245
	s_waitcnt lgkmcnt(1)
	v_add_f32_e32 v39, v39, v244
	s_waitcnt lgkmcnt(0)
	v_add_f32_e32 v40, v40, v245
	v_cndmask_b32_e64 v244, v40, v39, s[60:61]
	v_cndmask_b32_e64 v39, v39, v40, s[60:61]
	ds_bpermute_b32 v244, v105, v244
	s_waitcnt lgkmcnt(0)
	v_add_f32_e32 v39, v39, v244
	ds_bpermute_b32 v244, v110, v39
	s_waitcnt lgkmcnt(0)
	v_add_f32_e32 v2, v39, v244
	s_and_saveexec_b64 s[10:11], s[4:5]
	s_cbranch_execz .LBB0_121
	global_load_dword v78, v[32:33], off
	s_branch .Lp1_tail

.LBB0_585:
	s_ashr_i32 s5, s4, 31
	s_lshl_b64 s[14:15], s[4:5], 5
	s_add_u32 s14, s18, s14
	s_addc_u32 s15, s19, s15
	v_lshl_add_u64 v[20:21], s[14:15], 0, v[10:11]
	v_add_co_u32_e32 v22, vcc, 0x40000, v20
	global_load_dword v60, v10, s[14:15]
	s_nop 0
	v_addc_co_u32_e32 v23, vcc, 0, v21, vcc
	s_lshl_b64 s[14:15], s[4:5], 12
	v_add_co_u32_e32 v20, vcc, 0x80000, v20
	s_add_u32 s14, s96, s14
	s_nop 0
	v_addc_co_u32_e32 v21, vcc, 0, v21, vcc
	s_addc_u32 s15, s97, s15
	global_load_dword v61, v[22:23], off
	global_load_dword v62, v[20:21], off
	v_lshl_add_u64 v[20:21], s[14:15], 0, v[12:13]
	s_lshl_b64 s[14:15], s[4:5], 11
	v_lshl_or_b32 v22, v8, 1, s14
	v_mov_b32_e32 v23, s15
	v_lshl_add_u64 v[24:25], s[6:7], 0, v[22:23]
	v_lshl_add_u64 v[30:31], s[8:9], 0, v[22:23]
	v_lshl_add_u64 v[22:23], s[10:11], 0, v[22:23]
	global_load_dwordx4 v[26:29], v[24:25], off
	global_load_dwordx4 v[36:39], v[22:23], off
	global_load_dwordx4 v[32:35], v[30:31], off
	v_add_co_u32_e32 v40, vcc, s25, v20
	s_nop 1
	v_addc_co_u32_e32 v41, vcc, 0, v21, vcc
	global_load_dwordx4 v[40:43], v[40:41], off offset:2048
	s_nop 0
	global_load_dwordx4 v[44:47], v[24:25], off offset:16
	global_load_dwordx4 v[48:51], v[30:31], off offset:16
	global_load_dwordx4 v[52:55], v[22:23], off offset:16
	v_lshl_add_u64 v[20:21], v[20:21], 0, s[12:13]
	global_load_dwordx4 v[56:59], v[20:21], off offset:16
	s_waitcnt vmcnt(5)
	v_and_b32_e32 v63, 0xffff0000, v26
	v_max3_f32 v24, v60, v61, v62
	v_lshlrev_b32_e32 v30, 16, v26
	v_lshlrev_b32_e32 v25, 16, v32
	v_lshlrev_b32_e32 v31, 16, v36
	v_and_b32_e32 v26, 0xffff0000, v32
	v_and_b32_e32 v32, 0xffff0000, v36
	v_lshlrev_b32_e32 v36, 16, v27
	v_and_b32_e32 v65, 0xffff0000, v27
	v_and_b32_e32 v27, 0xffff0000, v33
	v_lshlrev_b32_e32 v67, 16, v34
	v_and_b32_e32 v69, 0xffff0000, v34
	v_sub_f32_e32 v34, v61, v24
	v_exp_f32_e32 v34, v34
	v_lshlrev_b32_e32 v64, 16, v37
	v_and_b32_e32 v66, 0xffff0000, v37
	v_lshlrev_b32_e32 v68, 16, v38
	v_and_b32_e32 v70, 0xffff0000, v38
	s_waitcnt vmcnt(4)
	v_lshlrev_b32_e32 v20, 16, v40
	v_and_b32_e32 v19, 0xffff0000, v40
	v_lshlrev_b32_e32 v40, 16, v33
	v_sub_f32_e32 v33, v60, v24
	v_sub_f32_e32 v24, v62, v24
	v_exp_f32_e32 v33, v33
	v_exp_f32_e32 v37, v24
	v_lshlrev_b32_e32 v62, 16, v35
	v_lshlrev_b32_e32 v22, 16, v41
	v_add_f32_e32 v38, v33, v34
	v_add_f32_e32 v38, v37, v38
	v_div_scale_f32 v60, s[16:17], v38, v38, 1.0
	v_rcp_f32_e32 v61, v60
	v_div_scale_f32 v71, vcc, 1.0, v38, 1.0
	v_and_b32_e32 v21, 0xffff0000, v41
	v_fma_f32 v72, -v60, v61, 1.0
	v_fmac_f32_e32 v61, v72, v61
	v_mul_f32_e32 v72, v71, v61
	v_fma_f32 v73, -v60, v72, v71
	v_fmac_f32_e32 v72, v73, v61
	v_fma_f32 v60, -v60, v72, v71
	v_div_fmas_f32 v60, v60, v61, v72
	v_div_fixup_f32 v38, v60, v38, 1.0
	v_mul_f32_e32 v61, v34, v38
	v_lshlrev_b32_e32 v41, 16, v28
	v_and_b32_e32 v28, 0xffff0000, v28
	v_lshlrev_b32_e32 v23, 16, v42
	v_and_b32_e32 v24, 0xffff0000, v42
	v_lshlrev_b32_e32 v42, 16, v29
	v_mul_f32_e32 v60, v33, v38
	v_mul_f32_e32 v71, v37, v38
	v_mul_f32_e32 v38, v61, v25
	v_mul_f32_e32 v37, v61, v26
	v_mul_f32_e32 v26, v61, v69
	v_mul_f32_e32 v25, v61, v62
	v_fmac_f32_e32 v26, v60, v28
	v_fmac_f32_e32 v25, v60, v42
	v_lshlrev_b32_e32 v28, 16, v39
	v_fmac_f32_e32 v25, v71, v28
	v_and_b32_e32 v28, 0xffff0000, v29
	v_and_b32_e32 v29, 0xffff0000, v35
	v_mul_f32_e32 v35, v61, v29
	v_fmac_f32_e32 v35, v60, v28
	v_and_b32_e32 v28, 0xffff0000, v39
	v_mul_f32_e32 v34, v61, v40
	v_mul_f32_e32 v33, v61, v27
	v_mul_f32_e32 v27, v61, v67
	v_fmac_f32_e32 v35, v71, v28
	s_waitcnt vmcnt(2)
	v_lshlrev_b32_e32 v28, 16, v48
	v_lshlrev_b32_e32 v40, 16, v49
	v_fmac_f32_e32 v38, v60, v30
	v_fmac_f32_e32 v37, v60, v63
	v_fmac_f32_e32 v27, v60, v41
	v_lshlrev_b32_e32 v30, 16, v44
	v_mul_f32_e32 v28, v61, v28
	v_mul_f32_e32 v41, v61, v40
	v_and_b32_e32 v40, 0xffff0000, v49
	v_lshlrev_b32_e32 v49, 16, v51
	v_fmac_f32_e32 v37, v71, v32
	v_fmac_f32_e32 v28, v60, v30
	s_waitcnt vmcnt(1)
	v_lshlrev_b32_e32 v30, 16, v52
	v_and_b32_e32 v32, 0xffff0000, v48
	v_lshlrev_b32_e32 v48, 16, v47
	v_mul_f32_e32 v49, v61, v49
	v_fmac_f32_e32 v34, v60, v36
	v_fmac_f32_e32 v28, v71, v30
	v_and_b32_e32 v30, 0xffff0000, v44
	v_mul_f32_e32 v36, v61, v32
	v_lshlrev_b32_e32 v39, 16, v45
	v_fmac_f32_e32 v49, v60, v48
	v_lshlrev_b32_e32 v48, 16, v55
	v_fmac_f32_e32 v38, v71, v31
	v_fmac_f32_e32 v36, v60, v30
	v_and_b32_e32 v30, 0xffff0000, v52
	v_fmac_f32_e32 v41, v60, v39
	v_lshlrev_b32_e32 v39, 16, v53
	v_fmac_f32_e32 v49, v71, v48
	v_and_b32_e32 v48, 0xffff0000, v51
	v_max_f32_e64 v51, |v20|, |v20|
	v_max_f32_e64 v52, |v19|, |v19|
	v_fmac_f32_e32 v33, v60, v65
	v_fmac_f32_e32 v41, v71, v39
	v_and_b32_e32 v39, 0xffff0000, v45
	v_mul_f32_e32 v45, v61, v40
	v_max_f32_e64 v51, |v38|, v51
	v_max_f32_e64 v52, |v37|, v52
	v_fmac_f32_e32 v34, v71, v64
	v_fmac_f32_e32 v33, v71, v66
	v_fmac_f32_e32 v45, v60, v39
	v_and_b32_e32 v39, 0xffff0000, v53
	v_max3_f32 v51, v51, 0, v52
	v_max_f32_e64 v52, |v22|, |v22|
	v_max_f32_e64 v53, |v21|, |v21|
	v_max_f32_e64 v52, |v34|, v52
	v_max_f32_e64 v53, |v33|, v53
	v_fmac_f32_e32 v27, v71, v68
	v_fmac_f32_e32 v26, v71, v70
	v_max3_f32 v51, v51, v52, v53
	v_max_f32_e64 v52, |v23|, |v23|
	v_max_f32_e64 v53, |v24|, |v24|
	v_lshlrev_b32_e32 v31, 16, v43
	v_and_b32_e32 v29, 0xffff0000, v43
	v_max_f32_e64 v52, |v27|, v52
	v_max_f32_e64 v53, |v26|, v53
	v_lshlrev_b32_e32 v40, 16, v50
	v_max3_f32 v51, v51, v52, v53
	v_max_f32_e64 v52, |v31|, |v31|
	v_max_f32_e64 v53, |v29|, |v29|
	v_fmac_f32_e32 v36, v71, v30
	s_waitcnt vmcnt(0)
	v_lshlrev_b32_e32 v32, 16, v56
	v_and_b32_e32 v30, 0xffff0000, v56
	v_fmac_f32_e32 v45, v71, v39
	v_lshlrev_b32_e32 v39, 16, v46
	v_mul_f32_e32 v42, v61, v40
	v_max_f32_e64 v52, |v25|, v52
	v_max_f32_e64 v53, |v35|, v53
	v_fmac_f32_e32 v42, v60, v39
	v_lshlrev_b32_e32 v39, 16, v54
	v_and_b32_e32 v40, 0xffff0000, v50
	v_max3_f32 v51, v51, v52, v53
	v_max_f32_e64 v52, |v32|, |v32|
	v_max_f32_e64 v53, |v30|, |v30|
	v_lshlrev_b32_e32 v44, 16, v57
	v_and_b32_e32 v43, 0xffff0000, v57
	v_fmac_f32_e32 v42, v71, v39
	v_and_b32_e32 v39, 0xffff0000, v46
	v_mul_f32_e32 v46, v61, v40
	v_max_f32_e64 v52, |v28|, v52
	v_max_f32_e64 v53, |v36|, v53
	v_fmac_f32_e32 v46, v60, v39
	v_and_b32_e32 v39, 0xffff0000, v54
	v_max3_f32 v51, v51, v52, v53
	v_max_f32_e64 v52, |v44|, |v44|
	v_max_f32_e64 v53, |v43|, |v43|
	v_fmac_f32_e32 v46, v71, v39
	v_lshlrev_b32_e32 v40, 16, v58
	v_and_b32_e32 v39, 0xffff0000, v58
	v_and_b32_e32 v47, 0xffff0000, v47
	v_mul_f32_e32 v50, v61, v48
	v_max_f32_e64 v52, |v41|, v52
	v_max_f32_e64 v53, |v45|, v53
	v_fmac_f32_e32 v50, v60, v47
	v_and_b32_e32 v47, 0xffff0000, v55
	v_max3_f32 v51, v51, v52, v53
	v_max_f32_e64 v52, |v40|, |v40|
	v_max_f32_e64 v53, |v39|, |v39|
	v_fmac_f32_e32 v50, v71, v47
	v_lshlrev_b32_e32 v48, 16, v59
	v_and_b32_e32 v47, 0xffff0000, v59
	v_max_f32_e64 v52, |v42|, v52
	v_max_f32_e64 v53, |v46|, v53
	v_max3_f32 v51, v51, v52, v53
	v_max_f32_e64 v52, |v48|, |v48|
	v_max_f32_e64 v53, |v47|, |v47|
	v_max_f32_e64 v52, |v49|, v52
	v_max_f32_e64 v53, |v50|, v53
	v_max3_f32 v51, v51, v52, v53
	ds_bpermute_b32 v52, v1, v51
	s_waitcnt lgkmcnt(0)
	v_max_f32_e32 v52, v52, v52
	v_max_f32_e32 v51, v51, v52
	ds_bpermute_b32 v52, v9, v51
	s_waitcnt lgkmcnt(0)
	v_max_f32_e32 v52, v52, v52
	v_max_f32_e32 v51, v51, v52
	ds_bpermute_b32 v52, v14, v51
	s_waitcnt lgkmcnt(0)
	v_max_f32_e32 v52, v52, v52
	v_max_f32_e32 v51, v51, v52
	ds_bpermute_b32 v52, v15, v51
	s_waitcnt lgkmcnt(0)
	v_max_f32_e32 v52, v52, v52
	v_max_f32_e32 v51, v51, v52
	ds_bpermute_b32 v52, v16, v51
	s_waitcnt lgkmcnt(0)
	v_max_f32_e32 v52, v52, v52
	v_max_f32_e32 v51, v51, v52
	ds_bpermute_b32 v52, v17, v51
	s_waitcnt lgkmcnt(0)
	v_max3_f32 v51, v51, v52, s26
	s_and_saveexec_b64 s[16:17], s[0:1]
	s_cbranch_execz .LBB0_584
	s_lshl_b64 s[34:35], s[4:5], 2
	s_add_u32 s34, s22, s34
	v_mul_f32_e32 v52, 0x3c010204, v51
	s_addc_u32 s35, s23, s35
	global_store_dword v3, v52, s[34:35]
	s_branch .LBB0_584
